# baseline (speedup 1.0000x reference)
_Z9feat_gemmPKDF16_S0_PDF16_:
	s_load_dwordx4 s[4:7], s[0:1], 0x8
	s_load_dwordx2 s[8:9], s[0:1], 0x0
	s_lshr_b32 s10, s2, 6
	s_lshl_b32 s10, s10, 3
	s_and_b32 s11, s2, 7
	s_or_b32 s10, s10, s11
	s_bfe_u32 s11, s2, 0x30003
	s_mul_i32 s12, s10, 0x44
	s_lshr_b32 s14, s12, 4
	s_lshl_b32 s15, s14, 3
	s_sub_u32 s15, 0x441, s15
	v_cvt_f32_u32_e32 v174, s15
	v_sqrt_f32_e32 v174, v174
	v_and_b32_e32 v170, 63, v0
	v_lshrrev_b32_e32 v171, 6, v0
	v_sub_f32_e32 v174, 0x42040000, v174
	v_fmaak_f32 v174, 0.5, v174, 0x3c23d70a
	v_cvt_u32_f32_e32 v174, v174
	v_lshlrev_b32_e32 v160, 4, v170
	v_readfirstlane_b32 s13, v174
	s_sub_u32 s15, 33, s13
	s_mul_i32 s15, s15, s13
	s_lshr_b32 s15, s15, 1
	s_sub_u32 s14, s14, s15
	s_add_u32 s14, s14, s13
	s_bfe_u32 s46, s12, 0x10003
	s_bfe_u32 s47, s12, 0x10002
	v_and_b32_e32 v172, 31, v170
	v_readfirstlane_b32 s33, v171
	v_lshrrev_b32_e32 v173, 5, v170
	s_lshl_b32 s35, s33, 12
	s_lshl_b32 s34, s11, 8
	s_lshl_b32 s36, s33, 5
	s_add_u32 s34, s34, s36
	v_add_lshl_u32 v165, v172, s34, 4
	v_add_u32_e32 v166, 0x8000, v165
	v_lshl_add_u32 v164, v173, 15, v165
	v_add_u32_e32 v168, s35, v160
	s_lshl_b32 s37, s47, 14
	v_add_u32_e32 v161, s37, v160
	s_waitcnt lgkmcnt(0)
	s_and_b32 s36, s12, 0xfff8
	s_lshl_b32 s36, s36, 12
	s_add_u32 s20, s4, s36
	s_addc_u32 s21, s5, 0
	s_min_u32 s43, s13, 15
	s_min_u32 s44, s14, 15
	s_lshl_b32 s45, s44, 16
	s_add_u32 s24, s8, s45
	s_addc_u32 s25, s9, 0
	s_add_u32 s26, s24, 0x100000
	s_addc_u32 s27, s25, 0
	s_lshl_b32 s45, s43, 16
	s_add_u32 s28, s8, s45
	s_addc_u32 s29, s9, 0
	s_add_u32 s30, s28, 0x100000
	s_addc_u32 s31, s29, 0
	global_load_dwordx4 v[36:39], v164, s[24:25]
	global_load_dwordx4 v[32:35], v164, s[26:27]
	global_load_dwordx4 v[40:43], v165, s[28:29]
	global_load_dwordx4 v[44:47], v166, s[28:29]
	global_load_dwordx4 v[48:51], v165, s[30:31]
	global_load_dwordx4 v[52:55], v166, s[30:31]
	s_mov_b32 s17, 17
	s_mov_b32 s18, 0
	s_mov_b32 s19, 0
	s_add_u32 m0, s18, s35
	s_add_u32 s18, s18, 0x8000
	global_load_lds_dwordx4 v168, s[20:21]
	global_load_lds_dwordx4 v168, s[20:21] offset:1024
	global_load_lds_dwordx4 v168, s[20:21] offset:2048
	global_load_lds_dwordx4 v168, s[20:21] offset:3072
	s_and_b32 s18, s18, 0x1ffff
	s_add_u32 s20, s20, 0x8000
	s_addc_u32 s21, s21, 0
	s_add_u32 m0, s18, s35
	s_add_u32 s18, s18, 0x8000
	global_load_lds_dwordx4 v168, s[20:21]
	global_load_lds_dwordx4 v168, s[20:21] offset:1024
	global_load_lds_dwordx4 v168, s[20:21] offset:2048
	global_load_lds_dwordx4 v168, s[20:21] offset:3072
	s_and_b32 s18, s18, 0x1ffff
	s_add_u32 s20, s20, 0x8000
	s_addc_u32 s21, s21, 0
	s_add_u32 m0, s18, s35
	s_add_u32 s18, s18, 0x8000
	global_load_lds_dwordx4 v168, s[20:21]
	global_load_lds_dwordx4 v168, s[20:21] offset:1024
	global_load_lds_dwordx4 v168, s[20:21] offset:2048
	global_load_lds_dwordx4 v168, s[20:21] offset:3072
	s_and_b32 s18, s18, 0x1ffff
	s_add_u32 s20, s20, 0x8000
	s_addc_u32 s21, s21, 0
	s_cmp_eq_u32 s46, 1
	s_cbranch_scc0 .Lk2_pro_a
	s_add_u32 s14, s14, 1
	s_cmp_eq_u32 s14, 16
	s_cselect_b32 s42, 1, 0
	s_add_u32 s13, s13, s42
	s_cmp_eq_u32 s42, 1
	s_cselect_b32 s14, s13, s14
	s_min_u32 s43, s13, 15
	s_min_u32 s44, s14, 15
	s_lshl_b32 s45, s44, 16
	s_add_u32 s24, s8, s45
	s_addc_u32 s25, s9, 0
	s_add_u32 s26, s24, 0x100000
	s_addc_u32 s27, s25, 0
	s_lshl_b32 s45, s43, 16
	s_add_u32 s28, s8, s45
	s_addc_u32 s29, s9, 0
	s_add_u32 s30, s28, 0x100000
	s_addc_u32 s31, s29, 0
	global_load_dwordx4 v[60:63], v164, s[24:25]
	global_load_dwordx4 v[56:59], v164, s[26:27]
	global_load_dwordx4 v[64:67], v165, s[28:29]
	global_load_dwordx4 v[68:71], v166, s[28:29]
	global_load_dwordx4 v[72:75], v165, s[30:31]
	global_load_dwordx4 v[76:79], v166, s[30:31]
.Lk2_pro_a:
	v_mov_b64_e32 v[0:1], 0
	v_mov_b64_e32 v[2:3], 0
	v_mov_b64_e32 v[4:5], 0
	v_mov_b64_e32 v[6:7], 0
	v_mov_b64_e32 v[8:9], 0
	v_mov_b64_e32 v[10:11], 0
	v_mov_b64_e32 v[12:13], 0
	v_mov_b64_e32 v[14:15], 0
	v_mov_b64_e32 v[16:17], 0
	v_mov_b64_e32 v[18:19], 0
	v_mov_b64_e32 v[20:21], 0
	v_mov_b64_e32 v[22:23], 0
	v_mov_b64_e32 v[24:25], 0
	v_mov_b64_e32 v[26:27], 0
	v_mov_b64_e32 v[28:29], 0
	v_mov_b64_e32 v[30:31], 0
	s_cmp_eq_u32 s46, 1
	s_cbranch_scc1 .Lk2_pro_w10
	s_waitcnt vmcnt(4)
	s_branch .Lk2_pro_bar
.Lk2_pro_w10:
	s_waitcnt vmcnt(10)
.Lk2_pro_bar:
	s_barrier
	s_cmp_eq_u32 s47, 1
	s_cbranch_scc0 .Lk2_pro_full
	s_add_u32 m0, s18, s35
	s_add_u32 s18, s18, 0x8000
	global_load_lds_dwordx4 v168, s[20:21]
	global_load_lds_dwordx4 v168, s[20:21] offset:1024
	global_load_lds_dwordx4 v168, s[20:21] offset:2048
	global_load_lds_dwordx4 v168, s[20:21] offset:3072
	s_and_b32 s18, s18, 0x1ffff
	s_add_u32 s20, s20, 0x8000
	s_addc_u32 s21, s21, 0
	s_cmp_eq_u32 s46, 0
	s_cbranch_scc0 .Lk2_pro_hb
	s_add_u32 s14, s14, 1
	s_cmp_eq_u32 s14, 16
	s_cselect_b32 s42, 1, 0
	s_add_u32 s13, s13, s42
	s_cmp_eq_u32 s42, 1
	s_cselect_b32 s14, s13, s14
	s_min_u32 s43, s13, 15
	s_min_u32 s44, s14, 15
	s_lshl_b32 s45, s44, 16
	s_add_u32 s24, s8, s45
	s_addc_u32 s25, s9, 0
	s_add_u32 s26, s24, 0x100000
	s_addc_u32 s27, s25, 0
	s_lshl_b32 s45, s43, 16
	s_add_u32 s28, s8, s45
	s_addc_u32 s29, s9, 0
	s_add_u32 s30, s28, 0x100000
	s_addc_u32 s31, s29, 0
	global_load_dwordx4 v[60:63], v164, s[24:25]
	global_load_dwordx4 v[56:59], v164, s[26:27]
	global_load_dwordx4 v[64:67], v165, s[28:29]
	global_load_dwordx4 v[68:71], v166, s[28:29]
	global_load_dwordx4 v[72:75], v165, s[30:31]
	global_load_dwordx4 v[76:79], v166, s[30:31]
.Lk2_pro_hb:
	ds_read_b128 v[80:83], v161
	ds_read_b128 v[84:87], v161 offset:1024
	ds_read_b128 v[88:91], v161 offset:2048
	ds_read_b128 v[92:95], v161 offset:3072
	ds_read_b128 v[96:99], v161 offset:4096
	ds_read_b128 v[100:103], v161 offset:5120
	ds_read_b128 v[104:107], v161 offset:6144
	ds_read_b128 v[108:111], v161 offset:7168
	s_cmp_eq_u32 s46, 0
	s_cbranch_scc1 .Lk2_eh0
.Lk2_eh1:
	v_pk_mul_f16 v144, v54, v32 op_sel:[0,0] op_sel_hi:[0,1]
	v_pk_mul_f16 v145, v54, v33 op_sel:[0,0] op_sel_hi:[0,1]
	v_pk_mul_f16 v146, v54, v34 op_sel:[0,0] op_sel_hi:[0,1]
	v_pk_mul_f16 v147, v54, v35 op_sel:[0,0] op_sel_hi:[0,1]
	v_pk_fma_f16 v144, v46, v36, v144 op_sel:[0,0,0] op_sel_hi:[0,1,1]
	v_pk_fma_f16 v145, v46, v37, v145 op_sel:[0,0,0] op_sel_hi:[0,1,1]
	v_pk_fma_f16 v146, v46, v38, v146 op_sel:[0,0,0] op_sel_hi:[0,1,1]
	v_pk_fma_f16 v147, v46, v39, v147 op_sel:[0,0,0] op_sel_hi:[0,1,1]
	v_pk_mul_f16 v148, v54, v36 op_sel:[0,0] op_sel_hi:[0,1]
	v_pk_mul_f16 v149, v54, v37 op_sel:[0,0] op_sel_hi:[0,1]
	v_pk_mul_f16 v150, v54, v38 op_sel:[0,0] op_sel_hi:[0,1]
	v_pk_mul_f16 v151, v54, v39 op_sel:[0,0] op_sel_hi:[0,1]
	v_pk_fma_f16 v148, v46, v32, v148 op_sel:[0,0,0] op_sel_hi:[0,1,1] neg_lo:[0,0,1] neg_hi:[0,0,1]
	v_pk_fma_f16 v149, v46, v33, v149 op_sel:[0,0,0] op_sel_hi:[0,1,1] neg_lo:[0,0,1] neg_hi:[0,0,1]
	v_pk_fma_f16 v150, v46, v34, v150 op_sel:[0,0,0] op_sel_hi:[0,1,1] neg_lo:[0,0,1] neg_hi:[0,0,1]
	v_pk_fma_f16 v151, v46, v35, v151 op_sel:[0,0,0] op_sel_hi:[0,1,1] neg_lo:[0,0,1] neg_hi:[0,0,1]
	v_mov_b32_e32 v161, v160
	s_nop 1
	s_branch .Lk2_h01
.Lk2_eh0:
	v_pk_mul_f16 v144, v50, v32 op_sel:[0,0] op_sel_hi:[0,1]
	v_pk_mul_f16 v145, v50, v33 op_sel:[0,0] op_sel_hi:[0,1]
	v_pk_mul_f16 v146, v50, v34 op_sel:[0,0] op_sel_hi:[0,1]
	v_pk_mul_f16 v147, v50, v35 op_sel:[0,0] op_sel_hi:[0,1]
	v_pk_fma_f16 v144, v42, v36, v144 op_sel:[0,0,0] op_sel_hi:[0,1,1]
	v_pk_fma_f16 v145, v42, v37, v145 op_sel:[0,0,0] op_sel_hi:[0,1,1]
	v_pk_fma_f16 v146, v42, v38, v146 op_sel:[0,0,0] op_sel_hi:[0,1,1]
	v_pk_fma_f16 v147, v42, v39, v147 op_sel:[0,0,0] op_sel_hi:[0,1,1]
	v_pk_mul_f16 v148, v50, v36 op_sel:[0,0] op_sel_hi:[0,1]
	v_pk_mul_f16 v149, v50, v37 op_sel:[0,0] op_sel_hi:[0,1]
	v_pk_mul_f16 v150, v50, v38 op_sel:[0,0] op_sel_hi:[0,1]
	v_pk_mul_f16 v151, v50, v39 op_sel:[0,0] op_sel_hi:[0,1]
	v_pk_fma_f16 v148, v42, v32, v148 op_sel:[0,0,0] op_sel_hi:[0,1,1] neg_lo:[0,0,1] neg_hi:[0,0,1]
	v_pk_fma_f16 v149, v42, v33, v149 op_sel:[0,0,0] op_sel_hi:[0,1,1] neg_lo:[0,0,1] neg_hi:[0,0,1]
	v_pk_fma_f16 v150, v42, v34, v150 op_sel:[0,0,0] op_sel_hi:[0,1,1] neg_lo:[0,0,1] neg_hi:[0,0,1]
	v_pk_fma_f16 v151, v42, v35, v151 op_sel:[0,0,0] op_sel_hi:[0,1,1] neg_lo:[0,0,1] neg_hi:[0,0,1]
	v_mov_b32_e32 v161, v160
	s_nop 1
	s_branch .Lk2_h00

.Lk2_e1:
	v_pk_mul_f16 v144, v52, v32 op_sel:[0,0] op_sel_hi:[0,1]
	v_pk_mul_f16 v145, v52, v33 op_sel:[0,0] op_sel_hi:[0,1]
	v_pk_mul_f16 v146, v52, v34 op_sel:[0,0] op_sel_hi:[0,1]
	v_pk_mul_f16 v147, v52, v35 op_sel:[0,0] op_sel_hi:[0,1]
	v_pk_fma_f16 v144, v44, v36, v144 op_sel:[0,0,0] op_sel_hi:[0,1,1]
	v_pk_fma_f16 v145, v44, v37, v145 op_sel:[0,0,0] op_sel_hi:[0,1,1]
	v_pk_fma_f16 v146, v44, v38, v146 op_sel:[0,0,0] op_sel_hi:[0,1,1]
	v_pk_fma_f16 v147, v44, v39, v147 op_sel:[0,0,0] op_sel_hi:[0,1,1]
	v_pk_mul_f16 v148, v52, v36 op_sel:[0,0] op_sel_hi:[0,1]
	v_pk_mul_f16 v149, v52, v37 op_sel:[0,0] op_sel_hi:[0,1]
	v_pk_mul_f16 v150, v52, v38 op_sel:[0,0] op_sel_hi:[0,1]
	v_pk_mul_f16 v151, v52, v39 op_sel:[0,0] op_sel_hi:[0,1]
	v_pk_fma_f16 v148, v44, v32, v148 op_sel:[0,0,0] op_sel_hi:[0,1,1] neg_lo:[0,0,1] neg_hi:[0,0,1]
	v_pk_fma_f16 v149, v44, v33, v149 op_sel:[0,0,0] op_sel_hi:[0,1,1] neg_lo:[0,0,1] neg_hi:[0,0,1]
	v_pk_fma_f16 v150, v44, v34, v150 op_sel:[0,0,0] op_sel_hi:[0,1,1] neg_lo:[0,0,1] neg_hi:[0,0,1]
	v_pk_fma_f16 v151, v44, v35, v151 op_sel:[0,0,0] op_sel_hi:[0,1,1] neg_lo:[0,0,1] neg_hi:[0,0,1]
	s_nop 1
	s_branch .Lk2_b01
.Lk2_e0:
	v_pk_mul_f16 v144, v48, v32 op_sel:[0,0] op_sel_hi:[0,1]
	v_pk_mul_f16 v145, v48, v33 op_sel:[0,0] op_sel_hi:[0,1]
	v_pk_mul_f16 v146, v48, v34 op_sel:[0,0] op_sel_hi:[0,1]
	v_pk_mul_f16 v147, v48, v35 op_sel:[0,0] op_sel_hi:[0,1]
	v_pk_fma_f16 v144, v40, v36, v144 op_sel:[0,0,0] op_sel_hi:[0,1,1]
	v_pk_fma_f16 v145, v40, v37, v145 op_sel:[0,0,0] op_sel_hi:[0,1,1]
	v_pk_fma_f16 v146, v40, v38, v146 op_sel:[0,0,0] op_sel_hi:[0,1,1]
	v_pk_fma_f16 v147, v40, v39, v147 op_sel:[0,0,0] op_sel_hi:[0,1,1]
	v_pk_mul_f16 v148, v48, v36 op_sel:[0,0] op_sel_hi:[0,1]
	v_pk_mul_f16 v149, v48, v37 op_sel:[0,0] op_sel_hi:[0,1]
	v_pk_mul_f16 v150, v48, v38 op_sel:[0,0] op_sel_hi:[0,1]
	v_pk_mul_f16 v151, v48, v39 op_sel:[0,0] op_sel_hi:[0,1]
	v_pk_fma_f16 v148, v40, v32, v148 op_sel:[0,0,0] op_sel_hi:[0,1,1] neg_lo:[0,0,1] neg_hi:[0,0,1]
	v_pk_fma_f16 v149, v40, v33, v149 op_sel:[0,0,0] op_sel_hi:[0,1,1] neg_lo:[0,0,1] neg_hi:[0,0,1]
	v_pk_fma_f16 v150, v40, v34, v150 op_sel:[0,0,0] op_sel_hi:[0,1,1] neg_lo:[0,0,1] neg_hi:[0,0,1]
	v_pk_fma_f16 v151, v40, v35, v151 op_sel:[0,0,0] op_sel_hi:[0,1,1] neg_lo:[0,0,1] neg_hi:[0,0,1]
	s_nop 1
	s_branch .Lk2_b00
.Lk2_s00:
	s_waitcnt vmcnt(10)
	s_barrier
.Lk2_b00:
	s_waitcnt lgkmcnt(4)
	v_mfma_f32_32x32x16_f16 v[16:31], v[144:147], v[80:83], v[16:31]
	s_add_u32 m0, s18, s35
	s_add_u32 s18, s18, 0x8000
	global_load_lds_dwordx4 v168, s[20:21]
	v_pk_mul_f16 v152, v48, v32 op_sel:[1,0] op_sel_hi:[1,1]
	v_pk_mul_f16 v153, v48, v33 op_sel:[1,0] op_sel_hi:[1,1]
	v_pk_mul_f16 v154, v48, v34 op_sel:[1,0] op_sel_hi:[1,1]
	v_pk_mul_f16 v155, v48, v35 op_sel:[1,0] op_sel_hi:[1,1]
	v_mfma_f32_32x32x16_f16 v[0:15], v[144:147], v[84:87], v[0:15]
	global_load_lds_dwordx4 v168, s[20:21] offset:1024
	global_load_lds_dwordx4 v168, s[20:21] offset:2048
	v_pk_fma_f16 v152, v40, v36, v152 op_sel:[1,0,0] op_sel_hi:[1,1,1]
	v_pk_fma_f16 v153, v40, v37, v153 op_sel:[1,0,0] op_sel_hi:[1,1,1]
	v_pk_fma_f16 v154, v40, v38, v154 op_sel:[1,0,0] op_sel_hi:[1,1,1]
	v_pk_fma_f16 v155, v40, v39, v155 op_sel:[1,0,0] op_sel_hi:[1,1,1]
	v_mfma_f32_32x32x16_f16 v[16:31], v[148:151], v[88:91], v[16:31]
	global_load_lds_dwordx4 v168, s[20:21] offset:3072
	s_and_b32 s18, s18, 0x1ffff
	v_pk_mul_f16 v156, v48, v36 op_sel:[1,0] op_sel_hi:[1,1]
	v_pk_mul_f16 v157, v48, v37 op_sel:[1,0] op_sel_hi:[1,1]
	v_pk_mul_f16 v158, v48, v38 op_sel:[1,0] op_sel_hi:[1,1]
	v_pk_mul_f16 v159, v48, v39 op_sel:[1,0] op_sel_hi:[1,1]
	v_mfma_f32_32x32x16_f16 v[0:15], v[148:151], v[92:95], v[0:15]
	s_add_u32 s20, s20, 0x8000
	s_addc_u32 s21, s21, 0
	v_pk_fma_f16 v156, v40, v32, v156 op_sel:[1,0,0] op_sel_hi:[1,1,1] neg_lo:[0,0,1] neg_hi:[0,0,1]
	v_pk_fma_f16 v157, v40, v33, v157 op_sel:[1,0,0] op_sel_hi:[1,1,1] neg_lo:[0,0,1] neg_hi:[0,0,1]
	v_pk_fma_f16 v158, v40, v34, v158 op_sel:[1,0,0] op_sel_hi:[1,1,1] neg_lo:[0,0,1] neg_hi:[0,0,1]
	v_pk_fma_f16 v159, v40, v35, v159 op_sel:[1,0,0] op_sel_hi:[1,1,1] neg_lo:[0,0,1] neg_hi:[0,0,1]
	ds_read_b128 v[112:115], v161 offset:8192
	ds_read_b128 v[116:119], v161 offset:9216
	ds_read_b128 v[120:123], v161 offset:10240
	ds_read_b128 v[124:127], v161 offset:11264
	s_waitcnt lgkmcnt(4)
	v_mfma_f32_32x32x16_f16 v[16:31], v[152:155], v[96:99], v[16:31]
	s_add_u32 s14, s14, 1
	s_cmp_eq_u32 s14, 16
	s_cselect_b32 s42, 1, 0
	s_add_u32 s13, s13, s42
	s_cmp_eq_u32 s42, 1
	s_cselect_b32 s14, s13, s14
	v_pk_mul_f16 v144, v49, v32 op_sel:[0,0] op_sel_hi:[0,1]
	v_pk_mul_f16 v145, v49, v33 op_sel:[0,0] op_sel_hi:[0,1]
	v_pk_mul_f16 v146, v49, v34 op_sel:[0,0] op_sel_hi:[0,1]
	v_pk_mul_f16 v147, v49, v35 op_sel:[0,0] op_sel_hi:[0,1]
	v_mfma_f32_32x32x16_f16 v[0:15], v[152:155], v[100:103], v[0:15]
	s_min_u32 s43, s13, 15
	s_min_u32 s44, s14, 15
	s_lshl_b32 s45, s44, 16
	v_pk_fma_f16 v144, v41, v36, v144 op_sel:[0,0,0] op_sel_hi:[0,1,1]
	v_pk_fma_f16 v145, v41, v37, v145 op_sel:[0,0,0] op_sel_hi:[0,1,1]
	v_pk_fma_f16 v146, v41, v38, v146 op_sel:[0,0,0] op_sel_hi:[0,1,1]
	v_pk_fma_f16 v147, v41, v39, v147 op_sel:[0,0,0] op_sel_hi:[0,1,1]
	v_mfma_f32_32x32x16_f16 v[16:31], v[156:159], v[104:107], v[16:31]
	s_add_u32 s24, s8, s45
	s_addc_u32 s25, s9, 0
	v_pk_mul_f16 v148, v49, v36 op_sel:[0,0] op_sel_hi:[0,1]
	v_pk_mul_f16 v149, v49, v37 op_sel:[0,0] op_sel_hi:[0,1]
	v_pk_mul_f16 v150, v49, v38 op_sel:[0,0] op_sel_hi:[0,1]
	v_pk_mul_f16 v151, v49, v39 op_sel:[0,0] op_sel_hi:[0,1]
	v_mfma_f32_32x32x16_f16 v[0:15], v[156:159], v[108:111], v[0:15]
	s_add_u32 s26, s24, 0x100000
	s_addc_u32 s27, s25, 0
	v_pk_fma_f16 v148, v41, v32, v148 op_sel:[0,0,0] op_sel_hi:[0,1,1] neg_lo:[0,0,1] neg_hi:[0,0,1]
	v_pk_fma_f16 v149, v41, v33, v149 op_sel:[0,0,0] op_sel_hi:[0,1,1] neg_lo:[0,0,1] neg_hi:[0,0,1]
	v_pk_fma_f16 v150, v41, v34, v150 op_sel:[0,0,0] op_sel_hi:[0,1,1] neg_lo:[0,0,1] neg_hi:[0,0,1]
	v_pk_fma_f16 v151, v41, v35, v151 op_sel:[0,0,0] op_sel_hi:[0,1,1] neg_lo:[0,0,1] neg_hi:[0,0,1]
	ds_read_b128 v[128:131], v161 offset:12288
	ds_read_b128 v[132:135], v161 offset:13312
	ds_read_b128 v[136:139], v161 offset:14336
	ds_read_b128 v[140:143], v161 offset:15360
	s_waitcnt lgkmcnt(4)
	v_mfma_f32_32x32x16_f16 v[16:31], v[144:147], v[112:115], v[16:31]
	s_lshl_b32 s45, s43, 16
	s_add_u32 s28, s8, s45
	s_addc_u32 s29, s9, 0
	v_pk_mul_f16 v152, v49, v32 op_sel:[1,0] op_sel_hi:[1,1]
	v_pk_mul_f16 v153, v49, v33 op_sel:[1,0] op_sel_hi:[1,1]
	v_pk_mul_f16 v154, v49, v34 op_sel:[1,0] op_sel_hi:[1,1]
	v_pk_mul_f16 v155, v49, v35 op_sel:[1,0] op_sel_hi:[1,1]
	v_mfma_f32_32x32x16_f16 v[0:15], v[144:147], v[116:119], v[0:15]
	s_add_u32 s30, s28, 0x100000
	s_addc_u32 s31, s29, 0
	v_pk_fma_f16 v152, v41, v36, v152 op_sel:[1,0,0] op_sel_hi:[1,1,1]
	v_pk_fma_f16 v153, v41, v37, v153 op_sel:[1,0,0] op_sel_hi:[1,1,1]
	v_pk_fma_f16 v154, v41, v38, v154 op_sel:[1,0,0] op_sel_hi:[1,1,1]
	v_pk_fma_f16 v155, v41, v39, v155 op_sel:[1,0,0] op_sel_hi:[1,1,1]
	v_mfma_f32_32x32x16_f16 v[16:31], v[148:151], v[120:123], v[16:31]
	global_load_dwordx4 v[60:63], v164, s[24:25]
	v_pk_mul_f16 v156, v49, v36 op_sel:[1,0] op_sel_hi:[1,1]
	v_pk_mul_f16 v157, v49, v37 op_sel:[1,0] op_sel_hi:[1,1]
	v_pk_mul_f16 v158, v49, v38 op_sel:[1,0] op_sel_hi:[1,1]
	v_pk_mul_f16 v159, v49, v39 op_sel:[1,0] op_sel_hi:[1,1]
	v_mfma_f32_32x32x16_f16 v[0:15], v[148:151], v[124:127], v[0:15]
	global_load_dwordx4 v[56:59], v164, s[26:27]
	v_pk_fma_f16 v156, v41, v32, v156 op_sel:[1,0,0] op_sel_hi:[1,1,1] neg_lo:[0,0,1] neg_hi:[0,0,1]
	v_pk_fma_f16 v157, v41, v33, v157 op_sel:[1,0,0] op_sel_hi:[1,1,1] neg_lo:[0,0,1] neg_hi:[0,0,1]
	v_pk_fma_f16 v158, v41, v34, v158 op_sel:[1,0,0] op_sel_hi:[1,1,1] neg_lo:[0,0,1] neg_hi:[0,0,1]
	v_pk_fma_f16 v159, v41, v35, v159 op_sel:[1,0,0] op_sel_hi:[1,1,1] neg_lo:[0,0,1] neg_hi:[0,0,1]
	ds_read_b128 v[80:83], v161 offset:16384
	ds_read_b128 v[84:87], v161 offset:17408
	ds_read_b128 v[88:91], v161 offset:18432
	ds_read_b128 v[92:95], v161 offset:19456
	s_waitcnt lgkmcnt(4)
	v_mfma_f32_32x32x16_f16 v[16:31], v[152:155], v[128:131], v[16:31]
	global_load_dwordx4 v[64:67], v165, s[28:29]
	v_pk_mul_f16 v144, v50, v32 op_sel:[0,0] op_sel_hi:[0,1]
	v_pk_mul_f16 v145, v50, v33 op_sel:[0,0] op_sel_hi:[0,1]
	v_pk_mul_f16 v146, v50, v34 op_sel:[0,0] op_sel_hi:[0,1]
	v_pk_mul_f16 v147, v50, v35 op_sel:[0,0] op_sel_hi:[0,1]
	v_mfma_f32_32x32x16_f16 v[0:15], v[152:155], v[132:135], v[0:15]
	global_load_dwordx4 v[68:71], v166, s[28:29]
	v_pk_fma_f16 v144, v42, v36, v144 op_sel:[0,0,0] op_sel_hi:[0,1,1]
	v_pk_fma_f16 v145, v42, v37, v145 op_sel:[0,0,0] op_sel_hi:[0,1,1]
	v_pk_fma_f16 v146, v42, v38, v146 op_sel:[0,0,0] op_sel_hi:[0,1,1]
	v_pk_fma_f16 v147, v42, v39, v147 op_sel:[0,0,0] op_sel_hi:[0,1,1]
	v_mfma_f32_32x32x16_f16 v[16:31], v[156:159], v[136:139], v[16:31]
	global_load_dwordx4 v[72:75], v165, s[30:31]
	v_pk_mul_f16 v148, v50, v36 op_sel:[0,0] op_sel_hi:[0,1]
	v_pk_mul_f16 v149, v50, v37 op_sel:[0,0] op_sel_hi:[0,1]
	v_pk_mul_f16 v150, v50, v38 op_sel:[0,0] op_sel_hi:[0,1]
	v_pk_mul_f16 v151, v50, v39 op_sel:[0,0] op_sel_hi:[0,1]
	v_mfma_f32_32x32x16_f16 v[0:15], v[156:159], v[140:143], v[0:15]
	global_load_dwordx4 v[76:79], v166, s[30:31]
	v_pk_fma_f16 v148, v42, v32, v148 op_sel:[0,0,0] op_sel_hi:[0,1,1] neg_lo:[0,0,1] neg_hi:[0,0,1]
	v_pk_fma_f16 v149, v42, v33, v149 op_sel:[0,0,0] op_sel_hi:[0,1,1] neg_lo:[0,0,1] neg_hi:[0,0,1]
	v_pk_fma_f16 v150, v42, v34, v150 op_sel:[0,0,0] op_sel_hi:[0,1,1] neg_lo:[0,0,1] neg_hi:[0,0,1]
	v_pk_fma_f16 v151, v42, v35, v151 op_sel:[0,0,0] op_sel_hi:[0,1,1] neg_lo:[0,0,1] neg_hi:[0,0,1]
	ds_read_b128 v[96:99], v161 offset:20480
	ds_read_b128 v[100:103], v161 offset:21504
	ds_read_b128 v[104:107], v161 offset:22528
	ds_read_b128 v[108:111], v161 offset:23552
	s_sub_u32 s17, s17, 1
	s_cmp_eq_u32 s17, 0
	s_cbranch_scc1 .Lk2_epi
.Lk2_h00:
	s_waitcnt lgkmcnt(4)
	v_mfma_f32_32x32x16_f16 v[16:31], v[144:147], v[80:83], v[16:31]
	v_pk_mul_f16 v152, v50, v32 op_sel:[1,0] op_sel_hi:[1,1]
	v_pk_mul_f16 v153, v50, v33 op_sel:[1,0] op_sel_hi:[1,1]
	v_pk_mul_f16 v154, v50, v34 op_sel:[1,0] op_sel_hi:[1,1]
	v_pk_mul_f16 v155, v50, v35 op_sel:[1,0] op_sel_hi:[1,1]
	v_mfma_f32_32x32x16_f16 v[0:15], v[144:147], v[84:87], v[0:15]
	v_pk_fma_f16 v152, v42, v36, v152 op_sel:[1,0,0] op_sel_hi:[1,1,1]
	v_pk_fma_f16 v153, v42, v37, v153 op_sel:[1,0,0] op_sel_hi:[1,1,1]
	v_pk_fma_f16 v154, v42, v38, v154 op_sel:[1,0,0] op_sel_hi:[1,1,1]
	v_pk_fma_f16 v155, v42, v39, v155 op_sel:[1,0,0] op_sel_hi:[1,1,1]
	v_mfma_f32_32x32x16_f16 v[16:31], v[148:151], v[88:91], v[16:31]
	v_pk_mul_f16 v156, v50, v36 op_sel:[1,0] op_sel_hi:[1,1]
	v_pk_mul_f16 v157, v50, v37 op_sel:[1,0] op_sel_hi:[1,1]
	v_pk_mul_f16 v158, v50, v38 op_sel:[1,0] op_sel_hi:[1,1]
	v_pk_mul_f16 v159, v50, v39 op_sel:[1,0] op_sel_hi:[1,1]
	v_mfma_f32_32x32x16_f16 v[0:15], v[148:151], v[92:95], v[0:15]
	v_pk_fma_f16 v156, v42, v32, v156 op_sel:[1,0,0] op_sel_hi:[1,1,1] neg_lo:[0,0,1] neg_hi:[0,0,1]
	v_pk_fma_f16 v157, v42, v33, v157 op_sel:[1,0,0] op_sel_hi:[1,1,1] neg_lo:[0,0,1] neg_hi:[0,0,1]
	v_pk_fma_f16 v158, v42, v34, v158 op_sel:[1,0,0] op_sel_hi:[1,1,1] neg_lo:[0,0,1] neg_hi:[0,0,1]
	v_pk_fma_f16 v159, v42, v35, v159 op_sel:[1,0,0] op_sel_hi:[1,1,1] neg_lo:[0,0,1] neg_hi:[0,0,1]
	ds_read_b128 v[112:115], v161 offset:24576
	ds_read_b128 v[116:119], v161 offset:25600
	ds_read_b128 v[120:123], v161 offset:26624
	ds_read_b128 v[124:127], v161 offset:27648
	s_waitcnt lgkmcnt(4)
	v_mfma_f32_32x32x16_f16 v[16:31], v[152:155], v[96:99], v[16:31]
	v_pk_mul_f16 v144, v51, v32 op_sel:[0,0] op_sel_hi:[0,1]
	v_pk_mul_f16 v145, v51, v33 op_sel:[0,0] op_sel_hi:[0,1]
	v_pk_mul_f16 v146, v51, v34 op_sel:[0,0] op_sel_hi:[0,1]
	v_pk_mul_f16 v147, v51, v35 op_sel:[0,0] op_sel_hi:[0,1]
	v_mfma_f32_32x32x16_f16 v[0:15], v[152:155], v[100:103], v[0:15]
	v_pk_fma_f16 v144, v43, v36, v144 op_sel:[0,0,0] op_sel_hi:[0,1,1]
	v_pk_fma_f16 v145, v43, v37, v145 op_sel:[0,0,0] op_sel_hi:[0,1,1]
	v_pk_fma_f16 v146, v43, v38, v146 op_sel:[0,0,0] op_sel_hi:[0,1,1]
	v_pk_fma_f16 v147, v43, v39, v147 op_sel:[0,0,0] op_sel_hi:[0,1,1]
	v_mfma_f32_32x32x16_f16 v[16:31], v[156:159], v[104:107], v[16:31]
	v_pk_mul_f16 v148, v51, v36 op_sel:[0,0] op_sel_hi:[0,1]
	v_pk_mul_f16 v149, v51, v37 op_sel:[0,0] op_sel_hi:[0,1]
	v_pk_mul_f16 v150, v51, v38 op_sel:[0,0] op_sel_hi:[0,1]
	v_pk_mul_f16 v151, v51, v39 op_sel:[0,0] op_sel_hi:[0,1]
	v_mfma_f32_32x32x16_f16 v[0:15], v[156:159], v[108:111], v[0:15]
	v_pk_fma_f16 v148, v43, v32, v148 op_sel:[0,0,0] op_sel_hi:[0,1,1] neg_lo:[0,0,1] neg_hi:[0,0,1]
	v_pk_fma_f16 v149, v43, v33, v149 op_sel:[0,0,0] op_sel_hi:[0,1,1] neg_lo:[0,0,1] neg_hi:[0,0,1]
	v_pk_fma_f16 v150, v43, v34, v150 op_sel:[0,0,0] op_sel_hi:[0,1,1] neg_lo:[0,0,1] neg_hi:[0,0,1]
	v_pk_fma_f16 v151, v43, v35, v151 op_sel:[0,0,0] op_sel_hi:[0,1,1] neg_lo:[0,0,1] neg_hi:[0,0,1]
	ds_read_b128 v[128:131], v161 offset:28672
	ds_read_b128 v[132:135], v161 offset:29696
	ds_read_b128 v[136:139], v161 offset:30720
	ds_read_b128 v[140:143], v161 offset:31744
	s_add_u32 s19, s19, 0x8000
	s_and_b32 s19, s19, 0x1ffff
	v_add_u32_e32 v161, s19, v160
	s_waitcnt lgkmcnt(4)
	v_mfma_f32_32x32x16_f16 v[16:31], v[144:147], v[112:115], v[16:31]
	v_pk_mul_f16 v152, v51, v32 op_sel:[1,0] op_sel_hi:[1,1]
	v_pk_mul_f16 v153, v51, v33 op_sel:[1,0] op_sel_hi:[1,1]
	v_pk_mul_f16 v154, v51, v34 op_sel:[1,0] op_sel_hi:[1,1]
	v_pk_mul_f16 v155, v51, v35 op_sel:[1,0] op_sel_hi:[1,1]
	v_mfma_f32_32x32x16_f16 v[0:15], v[144:147], v[116:119], v[0:15]
	v_pk_fma_f16 v152, v43, v36, v152 op_sel:[1,0,0] op_sel_hi:[1,1,1]
	v_pk_fma_f16 v153, v43, v37, v153 op_sel:[1,0,0] op_sel_hi:[1,1,1]
	v_pk_fma_f16 v154, v43, v38, v154 op_sel:[1,0,0] op_sel_hi:[1,1,1]
	v_pk_fma_f16 v155, v43, v39, v155 op_sel:[1,0,0] op_sel_hi:[1,1,1]
	v_mfma_f32_32x32x16_f16 v[16:31], v[148:151], v[120:123], v[16:31]
	v_pk_mul_f16 v156, v51, v36 op_sel:[1,0] op_sel_hi:[1,1]
	v_pk_mul_f16 v157, v51, v37 op_sel:[1,0] op_sel_hi:[1,1]
	v_pk_mul_f16 v158, v51, v38 op_sel:[1,0] op_sel_hi:[1,1]
	v_pk_mul_f16 v159, v51, v39 op_sel:[1,0] op_sel_hi:[1,1]
	v_mfma_f32_32x32x16_f16 v[0:15], v[148:151], v[124:127], v[0:15]
	v_pk_fma_f16 v156, v43, v32, v156 op_sel:[1,0,0] op_sel_hi:[1,1,1] neg_lo:[0,0,1] neg_hi:[0,0,1]
	v_pk_fma_f16 v157, v43, v33, v157 op_sel:[1,0,0] op_sel_hi:[1,1,1] neg_lo:[0,0,1] neg_hi:[0,0,1]
	v_pk_fma_f16 v158, v43, v34, v158 op_sel:[1,0,0] op_sel_hi:[1,1,1] neg_lo:[0,0,1] neg_hi:[0,0,1]
	v_pk_fma_f16 v159, v43, v35, v159 op_sel:[1,0,0] op_sel_hi:[1,1,1] neg_lo:[0,0,1] neg_hi:[0,0,1]
	ds_read_b128 v[80:83], v161
	ds_read_b128 v[84:87], v161 offset:1024
	ds_read_b128 v[88:91], v161 offset:2048
	ds_read_b128 v[92:95], v161 offset:3072
	s_waitcnt lgkmcnt(4)
	v_mfma_f32_32x32x16_f16 v[16:31], v[152:155], v[128:131], v[16:31]
	v_pk_mul_f16 v144, v52, v32 op_sel:[0,0] op_sel_hi:[0,1]
	v_pk_mul_f16 v145, v52, v33 op_sel:[0,0] op_sel_hi:[0,1]
	v_pk_mul_f16 v146, v52, v34 op_sel:[0,0] op_sel_hi:[0,1]
	v_pk_mul_f16 v147, v52, v35 op_sel:[0,0] op_sel_hi:[0,1]
	v_mfma_f32_32x32x16_f16 v[0:15], v[152:155], v[132:135], v[0:15]
	v_pk_fma_f16 v144, v44, v36, v144 op_sel:[0,0,0] op_sel_hi:[0,1,1]
	v_pk_fma_f16 v145, v44, v37, v145 op_sel:[0,0,0] op_sel_hi:[0,1,1]
	v_pk_fma_f16 v146, v44, v38, v146 op_sel:[0,0,0] op_sel_hi:[0,1,1]
	v_pk_fma_f16 v147, v44, v39, v147 op_sel:[0,0,0] op_sel_hi:[0,1,1]
	v_mfma_f32_32x32x16_f16 v[16:31], v[156:159], v[136:139], v[16:31]
	v_pk_mul_f16 v148, v52, v36 op_sel:[0,0] op_sel_hi:[0,1]
	v_pk_mul_f16 v149, v52, v37 op_sel:[0,0] op_sel_hi:[0,1]
	v_pk_mul_f16 v150, v52, v38 op_sel:[0,0] op_sel_hi:[0,1]
	v_pk_mul_f16 v151, v52, v39 op_sel:[0,0] op_sel_hi:[0,1]
	v_mfma_f32_32x32x16_f16 v[0:15], v[156:159], v[140:143], v[0:15]
	v_pk_fma_f16 v148, v44, v32, v148 op_sel:[0,0,0] op_sel_hi:[0,1,1] neg_lo:[0,0,1] neg_hi:[0,0,1]
	v_pk_fma_f16 v149, v44, v33, v149 op_sel:[0,0,0] op_sel_hi:[0,1,1] neg_lo:[0,0,1] neg_hi:[0,0,1]
	v_pk_fma_f16 v150, v44, v34, v150 op_sel:[0,0,0] op_sel_hi:[0,1,1] neg_lo:[0,0,1] neg_hi:[0,0,1]
	v_pk_fma_f16 v151, v44, v35, v151 op_sel:[0,0,0] op_sel_hi:[0,1,1] neg_lo:[0,0,1] neg_hi:[0,0,1]
	ds_read_b128 v[96:99], v161 offset:4096
	ds_read_b128 v[100:103], v161 offset:5120
	ds_read_b128 v[104:107], v161 offset:6144
	ds_read_b128 v[108:111], v161 offset:7168
	s_sub_u32 s17, s17, 1
	s_cmp_eq_u32 s17, 0
	s_cbranch_scc1 .Lk2_epi

.Lk2_b01:
	s_waitcnt lgkmcnt(4)
	v_mfma_f32_32x32x16_f16 v[16:31], v[144:147], v[80:83], v[16:31]
	s_add_u32 m0, s18, s35
	s_add_u32 s18, s18, 0x8000
	global_load_lds_dwordx4 v168, s[20:21]
	v_pk_mul_f16 v152, v52, v32 op_sel:[1,0] op_sel_hi:[1,1]
	v_pk_mul_f16 v153, v52, v33 op_sel:[1,0] op_sel_hi:[1,1]
	v_pk_mul_f16 v154, v52, v34 op_sel:[1,0] op_sel_hi:[1,1]
	v_pk_mul_f16 v155, v52, v35 op_sel:[1,0] op_sel_hi:[1,1]
	v_mfma_f32_32x32x16_f16 v[0:15], v[144:147], v[84:87], v[0:15]
	global_load_lds_dwordx4 v168, s[20:21] offset:1024
	global_load_lds_dwordx4 v168, s[20:21] offset:2048
	v_pk_fma_f16 v152, v44, v36, v152 op_sel:[1,0,0] op_sel_hi:[1,1,1]
	v_pk_fma_f16 v153, v44, v37, v153 op_sel:[1,0,0] op_sel_hi:[1,1,1]
	v_pk_fma_f16 v154, v44, v38, v154 op_sel:[1,0,0] op_sel_hi:[1,1,1]
	v_pk_fma_f16 v155, v44, v39, v155 op_sel:[1,0,0] op_sel_hi:[1,1,1]
	v_mfma_f32_32x32x16_f16 v[16:31], v[148:151], v[88:91], v[16:31]
	global_load_lds_dwordx4 v168, s[20:21] offset:3072
	s_and_b32 s18, s18, 0x1ffff
	v_pk_mul_f16 v156, v52, v36 op_sel:[1,0] op_sel_hi:[1,1]
	v_pk_mul_f16 v157, v52, v37 op_sel:[1,0] op_sel_hi:[1,1]
	v_pk_mul_f16 v158, v52, v38 op_sel:[1,0] op_sel_hi:[1,1]
	v_pk_mul_f16 v159, v52, v39 op_sel:[1,0] op_sel_hi:[1,1]
	v_mfma_f32_32x32x16_f16 v[0:15], v[148:151], v[92:95], v[0:15]
	s_add_u32 s20, s20, 0x8000
	s_addc_u32 s21, s21, 0
	v_pk_fma_f16 v156, v44, v32, v156 op_sel:[1,0,0] op_sel_hi:[1,1,1] neg_lo:[0,0,1] neg_hi:[0,0,1]
	v_pk_fma_f16 v157, v44, v33, v157 op_sel:[1,0,0] op_sel_hi:[1,1,1] neg_lo:[0,0,1] neg_hi:[0,0,1]
	v_pk_fma_f16 v158, v44, v34, v158 op_sel:[1,0,0] op_sel_hi:[1,1,1] neg_lo:[0,0,1] neg_hi:[0,0,1]
	v_pk_fma_f16 v159, v44, v35, v159 op_sel:[1,0,0] op_sel_hi:[1,1,1] neg_lo:[0,0,1] neg_hi:[0,0,1]
	ds_read_b128 v[112:115], v161 offset:8192
	ds_read_b128 v[116:119], v161 offset:9216
	ds_read_b128 v[120:123], v161 offset:10240
	ds_read_b128 v[124:127], v161 offset:11264
	s_waitcnt lgkmcnt(4)
	v_mfma_f32_32x32x16_f16 v[16:31], v[152:155], v[96:99], v[16:31]
	v_pk_mul_f16 v144, v53, v32 op_sel:[0,0] op_sel_hi:[0,1]
	v_pk_mul_f16 v145, v53, v33 op_sel:[0,0] op_sel_hi:[0,1]
	v_pk_mul_f16 v146, v53, v34 op_sel:[0,0] op_sel_hi:[0,1]
	v_pk_mul_f16 v147, v53, v35 op_sel:[0,0] op_sel_hi:[0,1]
	v_mfma_f32_32x32x16_f16 v[0:15], v[152:155], v[100:103], v[0:15]
	v_pk_fma_f16 v144, v45, v36, v144 op_sel:[0,0,0] op_sel_hi:[0,1,1]
	v_pk_fma_f16 v145, v45, v37, v145 op_sel:[0,0,0] op_sel_hi:[0,1,1]
	v_pk_fma_f16 v146, v45, v38, v146 op_sel:[0,0,0] op_sel_hi:[0,1,1]
	v_pk_fma_f16 v147, v45, v39, v147 op_sel:[0,0,0] op_sel_hi:[0,1,1]
	v_mfma_f32_32x32x16_f16 v[16:31], v[156:159], v[104:107], v[16:31]
	v_pk_mul_f16 v148, v53, v36 op_sel:[0,0] op_sel_hi:[0,1]
	v_pk_mul_f16 v149, v53, v37 op_sel:[0,0] op_sel_hi:[0,1]
	v_pk_mul_f16 v150, v53, v38 op_sel:[0,0] op_sel_hi:[0,1]
	v_pk_mul_f16 v151, v53, v39 op_sel:[0,0] op_sel_hi:[0,1]
	v_mfma_f32_32x32x16_f16 v[0:15], v[156:159], v[108:111], v[0:15]
	v_pk_fma_f16 v148, v45, v32, v148 op_sel:[0,0,0] op_sel_hi:[0,1,1] neg_lo:[0,0,1] neg_hi:[0,0,1]
	v_pk_fma_f16 v149, v45, v33, v149 op_sel:[0,0,0] op_sel_hi:[0,1,1] neg_lo:[0,0,1] neg_hi:[0,0,1]
	v_pk_fma_f16 v150, v45, v34, v150 op_sel:[0,0,0] op_sel_hi:[0,1,1] neg_lo:[0,0,1] neg_hi:[0,0,1]
	v_pk_fma_f16 v151, v45, v35, v151 op_sel:[0,0,0] op_sel_hi:[0,1,1] neg_lo:[0,0,1] neg_hi:[0,0,1]
	ds_read_b128 v[128:131], v161 offset:12288
	ds_read_b128 v[132:135], v161 offset:13312
	ds_read_b128 v[136:139], v161 offset:14336
	ds_read_b128 v[140:143], v161 offset:15360
	s_waitcnt lgkmcnt(4)
	v_mfma_f32_32x32x16_f16 v[16:31], v[144:147], v[112:115], v[16:31]
	v_pk_mul_f16 v152, v53, v32 op_sel:[1,0] op_sel_hi:[1,1]
	v_pk_mul_f16 v153, v53, v33 op_sel:[1,0] op_sel_hi:[1,1]
	v_pk_mul_f16 v154, v53, v34 op_sel:[1,0] op_sel_hi:[1,1]
	v_pk_mul_f16 v155, v53, v35 op_sel:[1,0] op_sel_hi:[1,1]
	v_mfma_f32_32x32x16_f16 v[0:15], v[144:147], v[116:119], v[0:15]
	v_pk_fma_f16 v152, v45, v36, v152 op_sel:[1,0,0] op_sel_hi:[1,1,1]
	v_pk_fma_f16 v153, v45, v37, v153 op_sel:[1,0,0] op_sel_hi:[1,1,1]
	v_pk_fma_f16 v154, v45, v38, v154 op_sel:[1,0,0] op_sel_hi:[1,1,1]
	v_pk_fma_f16 v155, v45, v39, v155 op_sel:[1,0,0] op_sel_hi:[1,1,1]
	v_mfma_f32_32x32x16_f16 v[16:31], v[148:151], v[120:123], v[16:31]
	v_pk_mul_f16 v156, v53, v36 op_sel:[1,0] op_sel_hi:[1,1]
	v_pk_mul_f16 v157, v53, v37 op_sel:[1,0] op_sel_hi:[1,1]
	v_pk_mul_f16 v158, v53, v38 op_sel:[1,0] op_sel_hi:[1,1]
	v_pk_mul_f16 v159, v53, v39 op_sel:[1,0] op_sel_hi:[1,1]
	v_mfma_f32_32x32x16_f16 v[0:15], v[148:151], v[124:127], v[0:15]
	v_pk_fma_f16 v156, v45, v32, v156 op_sel:[1,0,0] op_sel_hi:[1,1,1] neg_lo:[0,0,1] neg_hi:[0,0,1]
	v_pk_fma_f16 v157, v45, v33, v157 op_sel:[1,0,0] op_sel_hi:[1,1,1] neg_lo:[0,0,1] neg_hi:[0,0,1]
	v_pk_fma_f16 v158, v45, v34, v158 op_sel:[1,0,0] op_sel_hi:[1,1,1] neg_lo:[0,0,1] neg_hi:[0,0,1]
	v_pk_fma_f16 v159, v45, v35, v159 op_sel:[1,0,0] op_sel_hi:[1,1,1] neg_lo:[0,0,1] neg_hi:[0,0,1]
	ds_read_b128 v[80:83], v161 offset:16384
	ds_read_b128 v[84:87], v161 offset:17408
	ds_read_b128 v[88:91], v161 offset:18432
	ds_read_b128 v[92:95], v161 offset:19456
	s_waitcnt lgkmcnt(4)
	v_mfma_f32_32x32x16_f16 v[16:31], v[152:155], v[128:131], v[16:31]
	v_pk_mul_f16 v144, v54, v32 op_sel:[0,0] op_sel_hi:[0,1]
	v_pk_mul_f16 v145, v54, v33 op_sel:[0,0] op_sel_hi:[0,1]
	v_pk_mul_f16 v146, v54, v34 op_sel:[0,0] op_sel_hi:[0,1]
	v_pk_mul_f16 v147, v54, v35 op_sel:[0,0] op_sel_hi:[0,1]
	v_mfma_f32_32x32x16_f16 v[0:15], v[152:155], v[132:135], v[0:15]
	v_pk_fma_f16 v144, v46, v36, v144 op_sel:[0,0,0] op_sel_hi:[0,1,1]
	v_pk_fma_f16 v145, v46, v37, v145 op_sel:[0,0,0] op_sel_hi:[0,1,1]
	v_pk_fma_f16 v146, v46, v38, v146 op_sel:[0,0,0] op_sel_hi:[0,1,1]
	v_pk_fma_f16 v147, v46, v39, v147 op_sel:[0,0,0] op_sel_hi:[0,1,1]
	v_mfma_f32_32x32x16_f16 v[16:31], v[156:159], v[136:139], v[16:31]
	v_pk_mul_f16 v148, v54, v36 op_sel:[0,0] op_sel_hi:[0,1]
	v_pk_mul_f16 v149, v54, v37 op_sel:[0,0] op_sel_hi:[0,1]
	v_pk_mul_f16 v150, v54, v38 op_sel:[0,0] op_sel_hi:[0,1]
	v_pk_mul_f16 v151, v54, v39 op_sel:[0,0] op_sel_hi:[0,1]
	v_mfma_f32_32x32x16_f16 v[0:15], v[156:159], v[140:143], v[0:15]
	v_pk_fma_f16 v148, v46, v32, v148 op_sel:[0,0,0] op_sel_hi:[0,1,1] neg_lo:[0,0,1] neg_hi:[0,0,1]
	v_pk_fma_f16 v149, v46, v33, v149 op_sel:[0,0,0] op_sel_hi:[0,1,1] neg_lo:[0,0,1] neg_hi:[0,0,1]
	v_pk_fma_f16 v150, v46, v34, v150 op_sel:[0,0,0] op_sel_hi:[0,1,1] neg_lo:[0,0,1] neg_hi:[0,0,1]
	v_pk_fma_f16 v151, v46, v35, v151 op_sel:[0,0,0] op_sel_hi:[0,1,1] neg_lo:[0,0,1] neg_hi:[0,0,1]
	ds_read_b128 v[96:99], v161 offset:20480
	ds_read_b128 v[100:103], v161 offset:21504
	ds_read_b128 v[104:107], v161 offset:22528
	ds_read_b128 v[108:111], v161 offset:23552
	s_sub_u32 s17, s17, 1
	s_cmp_eq_u32 s17, 0
	s_cbranch_scc1 .Lk2_epi
.Lk2_h01:
	s_waitcnt lgkmcnt(4)
	v_mfma_f32_32x32x16_f16 v[16:31], v[144:147], v[80:83], v[16:31]
	v_pk_mul_f16 v152, v54, v32 op_sel:[1,0] op_sel_hi:[1,1]
	v_pk_mul_f16 v153, v54, v33 op_sel:[1,0] op_sel_hi:[1,1]
	v_pk_mul_f16 v154, v54, v34 op_sel:[1,0] op_sel_hi:[1,1]
	v_pk_mul_f16 v155, v54, v35 op_sel:[1,0] op_sel_hi:[1,1]
	v_mfma_f32_32x32x16_f16 v[0:15], v[144:147], v[84:87], v[0:15]
	v_pk_fma_f16 v152, v46, v36, v152 op_sel:[1,0,0] op_sel_hi:[1,1,1]
	v_pk_fma_f16 v153, v46, v37, v153 op_sel:[1,0,0] op_sel_hi:[1,1,1]
	v_pk_fma_f16 v154, v46, v38, v154 op_sel:[1,0,0] op_sel_hi:[1,1,1]
	v_pk_fma_f16 v155, v46, v39, v155 op_sel:[1,0,0] op_sel_hi:[1,1,1]
	v_mfma_f32_32x32x16_f16 v[16:31], v[148:151], v[88:91], v[16:31]
	v_pk_mul_f16 v156, v54, v36 op_sel:[1,0] op_sel_hi:[1,1]
	v_pk_mul_f16 v157, v54, v37 op_sel:[1,0] op_sel_hi:[1,1]
	v_pk_mul_f16 v158, v54, v38 op_sel:[1,0] op_sel_hi:[1,1]
	v_pk_mul_f16 v159, v54, v39 op_sel:[1,0] op_sel_hi:[1,1]
	v_mfma_f32_32x32x16_f16 v[0:15], v[148:151], v[92:95], v[0:15]
	v_pk_fma_f16 v156, v46, v32, v156 op_sel:[1,0,0] op_sel_hi:[1,1,1] neg_lo:[0,0,1] neg_hi:[0,0,1]
	v_pk_fma_f16 v157, v46, v33, v157 op_sel:[1,0,0] op_sel_hi:[1,1,1] neg_lo:[0,0,1] neg_hi:[0,0,1]
	v_pk_fma_f16 v158, v46, v34, v158 op_sel:[1,0,0] op_sel_hi:[1,1,1] neg_lo:[0,0,1] neg_hi:[0,0,1]
	v_pk_fma_f16 v159, v46, v35, v159 op_sel:[1,0,0] op_sel_hi:[1,1,1] neg_lo:[0,0,1] neg_hi:[0,0,1]
	ds_read_b128 v[112:115], v161 offset:24576
	ds_read_b128 v[116:119], v161 offset:25600
	ds_read_b128 v[120:123], v161 offset:26624
	ds_read_b128 v[124:127], v161 offset:27648
	s_waitcnt lgkmcnt(4)
	v_mfma_f32_32x32x16_f16 v[16:31], v[152:155], v[96:99], v[16:31]
	v_pk_mul_f16 v144, v55, v32 op_sel:[0,0] op_sel_hi:[0,1]
	v_pk_mul_f16 v145, v55, v33 op_sel:[0,0] op_sel_hi:[0,1]
	v_pk_mul_f16 v146, v55, v34 op_sel:[0,0] op_sel_hi:[0,1]
	v_pk_mul_f16 v147, v55, v35 op_sel:[0,0] op_sel_hi:[0,1]
	v_mfma_f32_32x32x16_f16 v[0:15], v[152:155], v[100:103], v[0:15]
	v_pk_fma_f16 v144, v47, v36, v144 op_sel:[0,0,0] op_sel_hi:[0,1,1]
	v_pk_fma_f16 v145, v47, v37, v145 op_sel:[0,0,0] op_sel_hi:[0,1,1]
	v_pk_fma_f16 v146, v47, v38, v146 op_sel:[0,0,0] op_sel_hi:[0,1,1]
	v_pk_fma_f16 v147, v47, v39, v147 op_sel:[0,0,0] op_sel_hi:[0,1,1]
	v_mfma_f32_32x32x16_f16 v[16:31], v[156:159], v[104:107], v[16:31]
	v_pk_mul_f16 v148, v55, v36 op_sel:[0,0] op_sel_hi:[0,1]
	v_pk_mul_f16 v149, v55, v37 op_sel:[0,0] op_sel_hi:[0,1]
	v_pk_mul_f16 v150, v55, v38 op_sel:[0,0] op_sel_hi:[0,1]
	v_pk_mul_f16 v151, v55, v39 op_sel:[0,0] op_sel_hi:[0,1]
	v_mfma_f32_32x32x16_f16 v[0:15], v[156:159], v[108:111], v[0:15]
	v_pk_fma_f16 v148, v47, v32, v148 op_sel:[0,0,0] op_sel_hi:[0,1,1] neg_lo:[0,0,1] neg_hi:[0,0,1]
	v_pk_fma_f16 v149, v47, v33, v149 op_sel:[0,0,0] op_sel_hi:[0,1,1] neg_lo:[0,0,1] neg_hi:[0,0,1]
	v_pk_fma_f16 v150, v47, v34, v150 op_sel:[0,0,0] op_sel_hi:[0,1,1] neg_lo:[0,0,1] neg_hi:[0,0,1]
	v_pk_fma_f16 v151, v47, v35, v151 op_sel:[0,0,0] op_sel_hi:[0,1,1] neg_lo:[0,0,1] neg_hi:[0,0,1]
	ds_read_b128 v[128:131], v161 offset:28672
	ds_read_b128 v[132:135], v161 offset:29696
	ds_read_b128 v[136:139], v161 offset:30720
	ds_read_b128 v[140:143], v161 offset:31744
	s_add_u32 s19, s19, 0x8000
	s_and_b32 s19, s19, 0x1ffff
	v_add_u32_e32 v161, s19, v160
	s_waitcnt lgkmcnt(4)
	v_mfma_f32_32x32x16_f16 v[16:31], v[144:147], v[112:115], v[16:31]
	v_pk_mul_f16 v152, v55, v32 op_sel:[1,0] op_sel_hi:[1,1]
	v_pk_mul_f16 v153, v55, v33 op_sel:[1,0] op_sel_hi:[1,1]
	v_pk_mul_f16 v154, v55, v34 op_sel:[1,0] op_sel_hi:[1,1]
	v_pk_mul_f16 v155, v55, v35 op_sel:[1,0] op_sel_hi:[1,1]
	v_mfma_f32_32x32x16_f16 v[0:15], v[144:147], v[116:119], v[0:15]
	v_pk_fma_f16 v152, v47, v36, v152 op_sel:[1,0,0] op_sel_hi:[1,1,1]
	v_pk_fma_f16 v153, v47, v37, v153 op_sel:[1,0,0] op_sel_hi:[1,1,1]
	v_pk_fma_f16 v154, v47, v38, v154 op_sel:[1,0,0] op_sel_hi:[1,1,1]
	v_pk_fma_f16 v155, v47, v39, v155 op_sel:[1,0,0] op_sel_hi:[1,1,1]
	v_mfma_f32_32x32x16_f16 v[16:31], v[148:151], v[120:123], v[16:31]
	v_pk_mul_f16 v156, v55, v36 op_sel:[1,0] op_sel_hi:[1,1]
	v_pk_mul_f16 v157, v55, v37 op_sel:[1,0] op_sel_hi:[1,1]
	v_pk_mul_f16 v158, v55, v38 op_sel:[1,0] op_sel_hi:[1,1]
	v_pk_mul_f16 v159, v55, v39 op_sel:[1,0] op_sel_hi:[1,1]
	v_mfma_f32_32x32x16_f16 v[0:15], v[148:151], v[124:127], v[0:15]
	v_pk_fma_f16 v156, v47, v32, v156 op_sel:[1,0,0] op_sel_hi:[1,1,1] neg_lo:[0,0,1] neg_hi:[0,0,1]
	v_pk_fma_f16 v157, v47, v33, v157 op_sel:[1,0,0] op_sel_hi:[1,1,1] neg_lo:[0,0,1] neg_hi:[0,0,1]
	v_pk_fma_f16 v158, v47, v34, v158 op_sel:[1,0,0] op_sel_hi:[1,1,1] neg_lo:[0,0,1] neg_hi:[0,0,1]
	v_pk_fma_f16 v159, v47, v35, v159 op_sel:[1,0,0] op_sel_hi:[1,1,1] neg_lo:[0,0,1] neg_hi:[0,0,1]
	ds_read_b128 v[80:83], v161
	ds_read_b128 v[84:87], v161 offset:1024
	ds_read_b128 v[88:91], v161 offset:2048
	ds_read_b128 v[92:95], v161 offset:3072
	s_waitcnt lgkmcnt(4)
	v_mfma_f32_32x32x16_f16 v[16:31], v[152:155], v[128:131], v[16:31]
	s_waitcnt vmcnt(4)
	v_pk_mul_f16 v144, v72, v56 op_sel:[0,0] op_sel_hi:[0,1]
	v_pk_mul_f16 v145, v72, v57 op_sel:[0,0] op_sel_hi:[0,1]
	v_pk_mul_f16 v146, v72, v58 op_sel:[0,0] op_sel_hi:[0,1]
	v_pk_mul_f16 v147, v72, v59 op_sel:[0,0] op_sel_hi:[0,1]
	v_mfma_f32_32x32x16_f16 v[0:15], v[152:155], v[132:135], v[0:15]
	v_pk_fma_f16 v144, v64, v60, v144 op_sel:[0,0,0] op_sel_hi:[0,1,1]
	v_pk_fma_f16 v145, v64, v61, v145 op_sel:[0,0,0] op_sel_hi:[0,1,1]
	v_pk_fma_f16 v146, v64, v62, v146 op_sel:[0,0,0] op_sel_hi:[0,1,1]
	v_pk_fma_f16 v147, v64, v63, v147 op_sel:[0,0,0] op_sel_hi:[0,1,1]
	v_mfma_f32_32x32x16_f16 v[16:31], v[156:159], v[136:139], v[16:31]
	v_pk_mul_f16 v148, v72, v60 op_sel:[0,0] op_sel_hi:[0,1]
	v_pk_mul_f16 v149, v72, v61 op_sel:[0,0] op_sel_hi:[0,1]
	v_pk_mul_f16 v150, v72, v62 op_sel:[0,0] op_sel_hi:[0,1]
	v_pk_mul_f16 v151, v72, v63 op_sel:[0,0] op_sel_hi:[0,1]
	v_mfma_f32_32x32x16_f16 v[0:15], v[156:159], v[140:143], v[0:15]
	v_pk_fma_f16 v148, v64, v56, v148 op_sel:[0,0,0] op_sel_hi:[0,1,1] neg_lo:[0,0,1] neg_hi:[0,0,1]
	v_pk_fma_f16 v149, v64, v57, v149 op_sel:[0,0,0] op_sel_hi:[0,1,1] neg_lo:[0,0,1] neg_hi:[0,0,1]
	v_pk_fma_f16 v150, v64, v58, v150 op_sel:[0,0,0] op_sel_hi:[0,1,1] neg_lo:[0,0,1] neg_hi:[0,0,1]
	v_pk_fma_f16 v151, v64, v59, v151 op_sel:[0,0,0] op_sel_hi:[0,1,1] neg_lo:[0,0,1] neg_hi:[0,0,1]
	ds_read_b128 v[96:99], v161 offset:4096
	ds_read_b128 v[100:103], v161 offset:5120
	ds_read_b128 v[104:107], v161 offset:6144
	ds_read_b128 v[108:111], v161 offset:7168
	s_sub_u32 s17, s17, 1
	s_cmp_eq_u32 s17, 0
	s_cbranch_scc1 .Lk2_epi

.Lk2_b10:
	s_waitcnt lgkmcnt(4)
	v_mfma_f32_32x32x16_f16 v[16:31], v[144:147], v[80:83], v[16:31]
	s_add_u32 m0, s18, s35
	s_add_u32 s18, s18, 0x8000
	global_load_lds_dwordx4 v168, s[20:21]
	v_pk_mul_f16 v152, v72, v56 op_sel:[1,0] op_sel_hi:[1,1]
	v_pk_mul_f16 v153, v72, v57 op_sel:[1,0] op_sel_hi:[1,1]
	v_pk_mul_f16 v154, v72, v58 op_sel:[1,0] op_sel_hi:[1,1]
	v_pk_mul_f16 v155, v72, v59 op_sel:[1,0] op_sel_hi:[1,1]
	v_mfma_f32_32x32x16_f16 v[0:15], v[144:147], v[84:87], v[0:15]
	global_load_lds_dwordx4 v168, s[20:21] offset:1024
	global_load_lds_dwordx4 v168, s[20:21] offset:2048
	v_pk_fma_f16 v152, v64, v60, v152 op_sel:[1,0,0] op_sel_hi:[1,1,1]
	v_pk_fma_f16 v153, v64, v61, v153 op_sel:[1,0,0] op_sel_hi:[1,1,1]
	v_pk_fma_f16 v154, v64, v62, v154 op_sel:[1,0,0] op_sel_hi:[1,1,1]
	v_pk_fma_f16 v155, v64, v63, v155 op_sel:[1,0,0] op_sel_hi:[1,1,1]
	v_mfma_f32_32x32x16_f16 v[16:31], v[148:151], v[88:91], v[16:31]
	global_load_lds_dwordx4 v168, s[20:21] offset:3072
	s_and_b32 s18, s18, 0x1ffff
	v_pk_mul_f16 v156, v72, v60 op_sel:[1,0] op_sel_hi:[1,1]
	v_pk_mul_f16 v157, v72, v61 op_sel:[1,0] op_sel_hi:[1,1]
	v_pk_mul_f16 v158, v72, v62 op_sel:[1,0] op_sel_hi:[1,1]
	v_pk_mul_f16 v159, v72, v63 op_sel:[1,0] op_sel_hi:[1,1]
	v_mfma_f32_32x32x16_f16 v[0:15], v[148:151], v[92:95], v[0:15]
	s_add_u32 s20, s20, 0x8000
	s_addc_u32 s21, s21, 0
	v_pk_fma_f16 v156, v64, v56, v156 op_sel:[1,0,0] op_sel_hi:[1,1,1] neg_lo:[0,0,1] neg_hi:[0,0,1]
	v_pk_fma_f16 v157, v64, v57, v157 op_sel:[1,0,0] op_sel_hi:[1,1,1] neg_lo:[0,0,1] neg_hi:[0,0,1]
	v_pk_fma_f16 v158, v64, v58, v158 op_sel:[1,0,0] op_sel_hi:[1,1,1] neg_lo:[0,0,1] neg_hi:[0,0,1]
	v_pk_fma_f16 v159, v64, v59, v159 op_sel:[1,0,0] op_sel_hi:[1,1,1] neg_lo:[0,0,1] neg_hi:[0,0,1]
	ds_read_b128 v[112:115], v161 offset:8192
	ds_read_b128 v[116:119], v161 offset:9216
	ds_read_b128 v[120:123], v161 offset:10240
	ds_read_b128 v[124:127], v161 offset:11264
	s_waitcnt lgkmcnt(4)
	v_mfma_f32_32x32x16_f16 v[16:31], v[152:155], v[96:99], v[16:31]
	s_add_u32 s14, s14, 1
	s_cmp_eq_u32 s14, 16
	s_cselect_b32 s42, 1, 0
	s_add_u32 s13, s13, s42
	s_cmp_eq_u32 s42, 1
	s_cselect_b32 s14, s13, s14
	v_pk_mul_f16 v144, v73, v56 op_sel:[0,0] op_sel_hi:[0,1]
	v_pk_mul_f16 v145, v73, v57 op_sel:[0,0] op_sel_hi:[0,1]
	v_pk_mul_f16 v146, v73, v58 op_sel:[0,0] op_sel_hi:[0,1]
	v_pk_mul_f16 v147, v73, v59 op_sel:[0,0] op_sel_hi:[0,1]
	v_mfma_f32_32x32x16_f16 v[0:15], v[152:155], v[100:103], v[0:15]
	s_min_u32 s43, s13, 15
	s_min_u32 s44, s14, 15
	s_lshl_b32 s45, s44, 16
	v_pk_fma_f16 v144, v65, v60, v144 op_sel:[0,0,0] op_sel_hi:[0,1,1]
	v_pk_fma_f16 v145, v65, v61, v145 op_sel:[0,0,0] op_sel_hi:[0,1,1]
	v_pk_fma_f16 v146, v65, v62, v146 op_sel:[0,0,0] op_sel_hi:[0,1,1]
	v_pk_fma_f16 v147, v65, v63, v147 op_sel:[0,0,0] op_sel_hi:[0,1,1]
	v_mfma_f32_32x32x16_f16 v[16:31], v[156:159], v[104:107], v[16:31]
	s_add_u32 s24, s8, s45
	s_addc_u32 s25, s9, 0
	v_pk_mul_f16 v148, v73, v60 op_sel:[0,0] op_sel_hi:[0,1]
	v_pk_mul_f16 v149, v73, v61 op_sel:[0,0] op_sel_hi:[0,1]
	v_pk_mul_f16 v150, v73, v62 op_sel:[0,0] op_sel_hi:[0,1]
	v_pk_mul_f16 v151, v73, v63 op_sel:[0,0] op_sel_hi:[0,1]
	v_mfma_f32_32x32x16_f16 v[0:15], v[156:159], v[108:111], v[0:15]
	s_add_u32 s26, s24, 0x100000
	s_addc_u32 s27, s25, 0
	v_pk_fma_f16 v148, v65, v56, v148 op_sel:[0,0,0] op_sel_hi:[0,1,1] neg_lo:[0,0,1] neg_hi:[0,0,1]
	v_pk_fma_f16 v149, v65, v57, v149 op_sel:[0,0,0] op_sel_hi:[0,1,1] neg_lo:[0,0,1] neg_hi:[0,0,1]
	v_pk_fma_f16 v150, v65, v58, v150 op_sel:[0,0,0] op_sel_hi:[0,1,1] neg_lo:[0,0,1] neg_hi:[0,0,1]
	v_pk_fma_f16 v151, v65, v59, v151 op_sel:[0,0,0] op_sel_hi:[0,1,1] neg_lo:[0,0,1] neg_hi:[0,0,1]
	ds_read_b128 v[128:131], v161 offset:12288
	ds_read_b128 v[132:135], v161 offset:13312
	ds_read_b128 v[136:139], v161 offset:14336
	ds_read_b128 v[140:143], v161 offset:15360
	s_waitcnt lgkmcnt(4)
	v_mfma_f32_32x32x16_f16 v[16:31], v[144:147], v[112:115], v[16:31]
	s_lshl_b32 s45, s43, 16
	s_add_u32 s28, s8, s45
	s_addc_u32 s29, s9, 0
	v_pk_mul_f16 v152, v73, v56 op_sel:[1,0] op_sel_hi:[1,1]
	v_pk_mul_f16 v153, v73, v57 op_sel:[1,0] op_sel_hi:[1,1]
	v_pk_mul_f16 v154, v73, v58 op_sel:[1,0] op_sel_hi:[1,1]
	v_pk_mul_f16 v155, v73, v59 op_sel:[1,0] op_sel_hi:[1,1]
	v_mfma_f32_32x32x16_f16 v[0:15], v[144:147], v[116:119], v[0:15]
	s_add_u32 s30, s28, 0x100000
	s_addc_u32 s31, s29, 0
	v_pk_fma_f16 v152, v65, v60, v152 op_sel:[1,0,0] op_sel_hi:[1,1,1]
	v_pk_fma_f16 v153, v65, v61, v153 op_sel:[1,0,0] op_sel_hi:[1,1,1]
	v_pk_fma_f16 v154, v65, v62, v154 op_sel:[1,0,0] op_sel_hi:[1,1,1]
	v_pk_fma_f16 v155, v65, v63, v155 op_sel:[1,0,0] op_sel_hi:[1,1,1]
	v_mfma_f32_32x32x16_f16 v[16:31], v[148:151], v[120:123], v[16:31]
	global_load_dwordx4 v[36:39], v164, s[24:25]
	v_pk_mul_f16 v156, v73, v60 op_sel:[1,0] op_sel_hi:[1,1]
	v_pk_mul_f16 v157, v73, v61 op_sel:[1,0] op_sel_hi:[1,1]
	v_pk_mul_f16 v158, v73, v62 op_sel:[1,0] op_sel_hi:[1,1]
	v_pk_mul_f16 v159, v73, v63 op_sel:[1,0] op_sel_hi:[1,1]
	v_mfma_f32_32x32x16_f16 v[0:15], v[148:151], v[124:127], v[0:15]
	global_load_dwordx4 v[32:35], v164, s[26:27]
	v_pk_fma_f16 v156, v65, v56, v156 op_sel:[1,0,0] op_sel_hi:[1,1,1] neg_lo:[0,0,1] neg_hi:[0,0,1]
	v_pk_fma_f16 v157, v65, v57, v157 op_sel:[1,0,0] op_sel_hi:[1,1,1] neg_lo:[0,0,1] neg_hi:[0,0,1]
	v_pk_fma_f16 v158, v65, v58, v158 op_sel:[1,0,0] op_sel_hi:[1,1,1] neg_lo:[0,0,1] neg_hi:[0,0,1]
	v_pk_fma_f16 v159, v65, v59, v159 op_sel:[1,0,0] op_sel_hi:[1,1,1] neg_lo:[0,0,1] neg_hi:[0,0,1]
	ds_read_b128 v[80:83], v161 offset:16384
	ds_read_b128 v[84:87], v161 offset:17408
	ds_read_b128 v[88:91], v161 offset:18432
	ds_read_b128 v[92:95], v161 offset:19456
	s_waitcnt lgkmcnt(4)
	v_mfma_f32_32x32x16_f16 v[16:31], v[152:155], v[128:131], v[16:31]
	global_load_dwordx4 v[40:43], v165, s[28:29]
	v_pk_mul_f16 v144, v74, v56 op_sel:[0,0] op_sel_hi:[0,1]
	v_pk_mul_f16 v145, v74, v57 op_sel:[0,0] op_sel_hi:[0,1]
	v_pk_mul_f16 v146, v74, v58 op_sel:[0,0] op_sel_hi:[0,1]
	v_pk_mul_f16 v147, v74, v59 op_sel:[0,0] op_sel_hi:[0,1]
	v_mfma_f32_32x32x16_f16 v[0:15], v[152:155], v[132:135], v[0:15]
	global_load_dwordx4 v[44:47], v166, s[28:29]
	v_pk_fma_f16 v144, v66, v60, v144 op_sel:[0,0,0] op_sel_hi:[0,1,1]
	v_pk_fma_f16 v145, v66, v61, v145 op_sel:[0,0,0] op_sel_hi:[0,1,1]
	v_pk_fma_f16 v146, v66, v62, v146 op_sel:[0,0,0] op_sel_hi:[0,1,1]
	v_pk_fma_f16 v147, v66, v63, v147 op_sel:[0,0,0] op_sel_hi:[0,1,1]
	v_mfma_f32_32x32x16_f16 v[16:31], v[156:159], v[136:139], v[16:31]
	global_load_dwordx4 v[48:51], v165, s[30:31]
	v_pk_mul_f16 v148, v74, v60 op_sel:[0,0] op_sel_hi:[0,1]
	v_pk_mul_f16 v149, v74, v61 op_sel:[0,0] op_sel_hi:[0,1]
	v_pk_mul_f16 v150, v74, v62 op_sel:[0,0] op_sel_hi:[0,1]
	v_pk_mul_f16 v151, v74, v63 op_sel:[0,0] op_sel_hi:[0,1]
	v_mfma_f32_32x32x16_f16 v[0:15], v[156:159], v[140:143], v[0:15]
	global_load_dwordx4 v[52:55], v166, s[30:31]
	v_pk_fma_f16 v148, v66, v56, v148 op_sel:[0,0,0] op_sel_hi:[0,1,1] neg_lo:[0,0,1] neg_hi:[0,0,1]
	v_pk_fma_f16 v149, v66, v57, v149 op_sel:[0,0,0] op_sel_hi:[0,1,1] neg_lo:[0,0,1] neg_hi:[0,0,1]
	v_pk_fma_f16 v150, v66, v58, v150 op_sel:[0,0,0] op_sel_hi:[0,1,1] neg_lo:[0,0,1] neg_hi:[0,0,1]
	v_pk_fma_f16 v151, v66, v59, v151 op_sel:[0,0,0] op_sel_hi:[0,1,1] neg_lo:[0,0,1] neg_hi:[0,0,1]
	ds_read_b128 v[96:99], v161 offset:20480
	ds_read_b128 v[100:103], v161 offset:21504
	ds_read_b128 v[104:107], v161 offset:22528
	ds_read_b128 v[108:111], v161 offset:23552
	s_sub_u32 s17, s17, 1
	s_cmp_eq_u32 s17, 0
	s_cbranch_scc1 .Lk2_epi
.Lk2_h10:
	s_waitcnt lgkmcnt(4)
	v_mfma_f32_32x32x16_f16 v[16:31], v[144:147], v[80:83], v[16:31]
	v_pk_mul_f16 v152, v74, v56 op_sel:[1,0] op_sel_hi:[1,1]
	v_pk_mul_f16 v153, v74, v57 op_sel:[1,0] op_sel_hi:[1,1]
	v_pk_mul_f16 v154, v74, v58 op_sel:[1,0] op_sel_hi:[1,1]
	v_pk_mul_f16 v155, v74, v59 op_sel:[1,0] op_sel_hi:[1,1]
	v_mfma_f32_32x32x16_f16 v[0:15], v[144:147], v[84:87], v[0:15]
	v_pk_fma_f16 v152, v66, v60, v152 op_sel:[1,0,0] op_sel_hi:[1,1,1]
	v_pk_fma_f16 v153, v66, v61, v153 op_sel:[1,0,0] op_sel_hi:[1,1,1]
	v_pk_fma_f16 v154, v66, v62, v154 op_sel:[1,0,0] op_sel_hi:[1,1,1]
	v_pk_fma_f16 v155, v66, v63, v155 op_sel:[1,0,0] op_sel_hi:[1,1,1]
	v_mfma_f32_32x32x16_f16 v[16:31], v[148:151], v[88:91], v[16:31]
	v_pk_mul_f16 v156, v74, v60 op_sel:[1,0] op_sel_hi:[1,1]
	v_pk_mul_f16 v157, v74, v61 op_sel:[1,0] op_sel_hi:[1,1]
	v_pk_mul_f16 v158, v74, v62 op_sel:[1,0] op_sel_hi:[1,1]
	v_pk_mul_f16 v159, v74, v63 op_sel:[1,0] op_sel_hi:[1,1]
	v_mfma_f32_32x32x16_f16 v[0:15], v[148:151], v[92:95], v[0:15]
	v_pk_fma_f16 v156, v66, v56, v156 op_sel:[1,0,0] op_sel_hi:[1,1,1] neg_lo:[0,0,1] neg_hi:[0,0,1]
	v_pk_fma_f16 v157, v66, v57, v157 op_sel:[1,0,0] op_sel_hi:[1,1,1] neg_lo:[0,0,1] neg_hi:[0,0,1]
	v_pk_fma_f16 v158, v66, v58, v158 op_sel:[1,0,0] op_sel_hi:[1,1,1] neg_lo:[0,0,1] neg_hi:[0,0,1]
	v_pk_fma_f16 v159, v66, v59, v159 op_sel:[1,0,0] op_sel_hi:[1,1,1] neg_lo:[0,0,1] neg_hi:[0,0,1]
	ds_read_b128 v[112:115], v161 offset:24576
	ds_read_b128 v[116:119], v161 offset:25600
	ds_read_b128 v[120:123], v161 offset:26624
	ds_read_b128 v[124:127], v161 offset:27648
	s_waitcnt lgkmcnt(4)
	v_mfma_f32_32x32x16_f16 v[16:31], v[152:155], v[96:99], v[16:31]
	v_pk_mul_f16 v144, v75, v56 op_sel:[0,0] op_sel_hi:[0,1]
	v_pk_mul_f16 v145, v75, v57 op_sel:[0,0] op_sel_hi:[0,1]
	v_pk_mul_f16 v146, v75, v58 op_sel:[0,0] op_sel_hi:[0,1]
	v_pk_mul_f16 v147, v75, v59 op_sel:[0,0] op_sel_hi:[0,1]
	v_mfma_f32_32x32x16_f16 v[0:15], v[152:155], v[100:103], v[0:15]
	v_pk_fma_f16 v144, v67, v60, v144 op_sel:[0,0,0] op_sel_hi:[0,1,1]
	v_pk_fma_f16 v145, v67, v61, v145 op_sel:[0,0,0] op_sel_hi:[0,1,1]
	v_pk_fma_f16 v146, v67, v62, v146 op_sel:[0,0,0] op_sel_hi:[0,1,1]
	v_pk_fma_f16 v147, v67, v63, v147 op_sel:[0,0,0] op_sel_hi:[0,1,1]
	v_mfma_f32_32x32x16_f16 v[16:31], v[156:159], v[104:107], v[16:31]
	v_pk_mul_f16 v148, v75, v60 op_sel:[0,0] op_sel_hi:[0,1]
	v_pk_mul_f16 v149, v75, v61 op_sel:[0,0] op_sel_hi:[0,1]
	v_pk_mul_f16 v150, v75, v62 op_sel:[0,0] op_sel_hi:[0,1]
	v_pk_mul_f16 v151, v75, v63 op_sel:[0,0] op_sel_hi:[0,1]
	v_mfma_f32_32x32x16_f16 v[0:15], v[156:159], v[108:111], v[0:15]
	v_pk_fma_f16 v148, v67, v56, v148 op_sel:[0,0,0] op_sel_hi:[0,1,1] neg_lo:[0,0,1] neg_hi:[0,0,1]
	v_pk_fma_f16 v149, v67, v57, v149 op_sel:[0,0,0] op_sel_hi:[0,1,1] neg_lo:[0,0,1] neg_hi:[0,0,1]
	v_pk_fma_f16 v150, v67, v58, v150 op_sel:[0,0,0] op_sel_hi:[0,1,1] neg_lo:[0,0,1] neg_hi:[0,0,1]
	v_pk_fma_f16 v151, v67, v59, v151 op_sel:[0,0,0] op_sel_hi:[0,1,1] neg_lo:[0,0,1] neg_hi:[0,0,1]
	ds_read_b128 v[128:131], v161 offset:28672
	ds_read_b128 v[132:135], v161 offset:29696
	ds_read_b128 v[136:139], v161 offset:30720
	ds_read_b128 v[140:143], v161 offset:31744
	s_add_u32 s19, s19, 0x8000
	s_and_b32 s19, s19, 0x1ffff
	v_add_u32_e32 v161, s19, v160
	s_waitcnt lgkmcnt(4)
	v_mfma_f32_32x32x16_f16 v[16:31], v[144:147], v[112:115], v[16:31]
	v_pk_mul_f16 v152, v75, v56 op_sel:[1,0] op_sel_hi:[1,1]
	v_pk_mul_f16 v153, v75, v57 op_sel:[1,0] op_sel_hi:[1,1]
	v_pk_mul_f16 v154, v75, v58 op_sel:[1,0] op_sel_hi:[1,1]
	v_pk_mul_f16 v155, v75, v59 op_sel:[1,0] op_sel_hi:[1,1]
	v_mfma_f32_32x32x16_f16 v[0:15], v[144:147], v[116:119], v[0:15]
	v_pk_fma_f16 v152, v67, v60, v152 op_sel:[1,0,0] op_sel_hi:[1,1,1]
	v_pk_fma_f16 v153, v67, v61, v153 op_sel:[1,0,0] op_sel_hi:[1,1,1]
	v_pk_fma_f16 v154, v67, v62, v154 op_sel:[1,0,0] op_sel_hi:[1,1,1]
	v_pk_fma_f16 v155, v67, v63, v155 op_sel:[1,0,0] op_sel_hi:[1,1,1]
	v_mfma_f32_32x32x16_f16 v[16:31], v[148:151], v[120:123], v[16:31]
	v_pk_mul_f16 v156, v75, v60 op_sel:[1,0] op_sel_hi:[1,1]
	v_pk_mul_f16 v157, v75, v61 op_sel:[1,0] op_sel_hi:[1,1]
	v_pk_mul_f16 v158, v75, v62 op_sel:[1,0] op_sel_hi:[1,1]
	v_pk_mul_f16 v159, v75, v63 op_sel:[1,0] op_sel_hi:[1,1]
	v_mfma_f32_32x32x16_f16 v[0:15], v[148:151], v[124:127], v[0:15]
	v_pk_fma_f16 v156, v67, v56, v156 op_sel:[1,0,0] op_sel_hi:[1,1,1] neg_lo:[0,0,1] neg_hi:[0,0,1]
	v_pk_fma_f16 v157, v67, v57, v157 op_sel:[1,0,0] op_sel_hi:[1,1,1] neg_lo:[0,0,1] neg_hi:[0,0,1]
	v_pk_fma_f16 v158, v67, v58, v158 op_sel:[1,0,0] op_sel_hi:[1,1,1] neg_lo:[0,0,1] neg_hi:[0,0,1]
	v_pk_fma_f16 v159, v67, v59, v159 op_sel:[1,0,0] op_sel_hi:[1,1,1] neg_lo:[0,0,1] neg_hi:[0,0,1]
	ds_read_b128 v[80:83], v161
	ds_read_b128 v[84:87], v161 offset:1024
	ds_read_b128 v[88:91], v161 offset:2048
	ds_read_b128 v[92:95], v161 offset:3072
	s_waitcnt lgkmcnt(4)
	v_mfma_f32_32x32x16_f16 v[16:31], v[152:155], v[128:131], v[16:31]
	v_pk_mul_f16 v144, v76, v56 op_sel:[0,0] op_sel_hi:[0,1]
	v_pk_mul_f16 v145, v76, v57 op_sel:[0,0] op_sel_hi:[0,1]
	v_pk_mul_f16 v146, v76, v58 op_sel:[0,0] op_sel_hi:[0,1]
	v_pk_mul_f16 v147, v76, v59 op_sel:[0,0] op_sel_hi:[0,1]
	v_mfma_f32_32x32x16_f16 v[0:15], v[152:155], v[132:135], v[0:15]
	v_pk_fma_f16 v144, v68, v60, v144 op_sel:[0,0,0] op_sel_hi:[0,1,1]
	v_pk_fma_f16 v145, v68, v61, v145 op_sel:[0,0,0] op_sel_hi:[0,1,1]
	v_pk_fma_f16 v146, v68, v62, v146 op_sel:[0,0,0] op_sel_hi:[0,1,1]
	v_pk_fma_f16 v147, v68, v63, v147 op_sel:[0,0,0] op_sel_hi:[0,1,1]
	v_mfma_f32_32x32x16_f16 v[16:31], v[156:159], v[136:139], v[16:31]
	v_pk_mul_f16 v148, v76, v60 op_sel:[0,0] op_sel_hi:[0,1]
	v_pk_mul_f16 v149, v76, v61 op_sel:[0,0] op_sel_hi:[0,1]
	v_pk_mul_f16 v150, v76, v62 op_sel:[0,0] op_sel_hi:[0,1]
	v_pk_mul_f16 v151, v76, v63 op_sel:[0,0] op_sel_hi:[0,1]
	v_mfma_f32_32x32x16_f16 v[0:15], v[156:159], v[140:143], v[0:15]
	v_pk_fma_f16 v148, v68, v56, v148 op_sel:[0,0,0] op_sel_hi:[0,1,1] neg_lo:[0,0,1] neg_hi:[0,0,1]
	v_pk_fma_f16 v149, v68, v57, v149 op_sel:[0,0,0] op_sel_hi:[0,1,1] neg_lo:[0,0,1] neg_hi:[0,0,1]
	v_pk_fma_f16 v150, v68, v58, v150 op_sel:[0,0,0] op_sel_hi:[0,1,1] neg_lo:[0,0,1] neg_hi:[0,0,1]
	v_pk_fma_f16 v151, v68, v59, v151 op_sel:[0,0,0] op_sel_hi:[0,1,1] neg_lo:[0,0,1] neg_hi:[0,0,1]
	ds_read_b128 v[96:99], v161 offset:4096
	ds_read_b128 v[100:103], v161 offset:5120
	ds_read_b128 v[104:107], v161 offset:6144
	ds_read_b128 v[108:111], v161 offset:7168
	s_sub_u32 s17, s17, 1
	s_cmp_eq_u32 s17, 0
	s_cbranch_scc1 .Lk2_epi

.Lk2_b11:
	s_waitcnt lgkmcnt(4)
	v_mfma_f32_32x32x16_f16 v[16:31], v[144:147], v[80:83], v[16:31]
	s_add_u32 m0, s18, s35
	s_add_u32 s18, s18, 0x8000
	global_load_lds_dwordx4 v168, s[20:21]
	v_pk_mul_f16 v152, v76, v56 op_sel:[1,0] op_sel_hi:[1,1]
	v_pk_mul_f16 v153, v76, v57 op_sel:[1,0] op_sel_hi:[1,1]
	v_pk_mul_f16 v154, v76, v58 op_sel:[1,0] op_sel_hi:[1,1]
	v_pk_mul_f16 v155, v76, v59 op_sel:[1,0] op_sel_hi:[1,1]
	v_mfma_f32_32x32x16_f16 v[0:15], v[144:147], v[84:87], v[0:15]
	global_load_lds_dwordx4 v168, s[20:21] offset:1024
	global_load_lds_dwordx4 v168, s[20:21] offset:2048
	v_pk_fma_f16 v152, v68, v60, v152 op_sel:[1,0,0] op_sel_hi:[1,1,1]
	v_pk_fma_f16 v153, v68, v61, v153 op_sel:[1,0,0] op_sel_hi:[1,1,1]
	v_pk_fma_f16 v154, v68, v62, v154 op_sel:[1,0,0] op_sel_hi:[1,1,1]
	v_pk_fma_f16 v155, v68, v63, v155 op_sel:[1,0,0] op_sel_hi:[1,1,1]
	v_mfma_f32_32x32x16_f16 v[16:31], v[148:151], v[88:91], v[16:31]
	global_load_lds_dwordx4 v168, s[20:21] offset:3072
	s_and_b32 s18, s18, 0x1ffff
	v_pk_mul_f16 v156, v76, v60 op_sel:[1,0] op_sel_hi:[1,1]
	v_pk_mul_f16 v157, v76, v61 op_sel:[1,0] op_sel_hi:[1,1]
	v_pk_mul_f16 v158, v76, v62 op_sel:[1,0] op_sel_hi:[1,1]
	v_pk_mul_f16 v159, v76, v63 op_sel:[1,0] op_sel_hi:[1,1]
	v_mfma_f32_32x32x16_f16 v[0:15], v[148:151], v[92:95], v[0:15]
	s_add_u32 s20, s20, 0x8000
	s_addc_u32 s21, s21, 0
	v_pk_fma_f16 v156, v68, v56, v156 op_sel:[1,0,0] op_sel_hi:[1,1,1] neg_lo:[0,0,1] neg_hi:[0,0,1]
	v_pk_fma_f16 v157, v68, v57, v157 op_sel:[1,0,0] op_sel_hi:[1,1,1] neg_lo:[0,0,1] neg_hi:[0,0,1]
	v_pk_fma_f16 v158, v68, v58, v158 op_sel:[1,0,0] op_sel_hi:[1,1,1] neg_lo:[0,0,1] neg_hi:[0,0,1]
	v_pk_fma_f16 v159, v68, v59, v159 op_sel:[1,0,0] op_sel_hi:[1,1,1] neg_lo:[0,0,1] neg_hi:[0,0,1]
	ds_read_b128 v[112:115], v161 offset:8192
	ds_read_b128 v[116:119], v161 offset:9216
	ds_read_b128 v[120:123], v161 offset:10240
	ds_read_b128 v[124:127], v161 offset:11264
	s_waitcnt lgkmcnt(4)
	v_mfma_f32_32x32x16_f16 v[16:31], v[152:155], v[96:99], v[16:31]
	v_pk_mul_f16 v144, v77, v56 op_sel:[0,0] op_sel_hi:[0,1]
	v_pk_mul_f16 v145, v77, v57 op_sel:[0,0] op_sel_hi:[0,1]
	v_pk_mul_f16 v146, v77, v58 op_sel:[0,0] op_sel_hi:[0,1]
	v_pk_mul_f16 v147, v77, v59 op_sel:[0,0] op_sel_hi:[0,1]
	v_mfma_f32_32x32x16_f16 v[0:15], v[152:155], v[100:103], v[0:15]
	v_pk_fma_f16 v144, v69, v60, v144 op_sel:[0,0,0] op_sel_hi:[0,1,1]
	v_pk_fma_f16 v145, v69, v61, v145 op_sel:[0,0,0] op_sel_hi:[0,1,1]
	v_pk_fma_f16 v146, v69, v62, v146 op_sel:[0,0,0] op_sel_hi:[0,1,1]
	v_pk_fma_f16 v147, v69, v63, v147 op_sel:[0,0,0] op_sel_hi:[0,1,1]
	v_mfma_f32_32x32x16_f16 v[16:31], v[156:159], v[104:107], v[16:31]
	v_pk_mul_f16 v148, v77, v60 op_sel:[0,0] op_sel_hi:[0,1]
	v_pk_mul_f16 v149, v77, v61 op_sel:[0,0] op_sel_hi:[0,1]
	v_pk_mul_f16 v150, v77, v62 op_sel:[0,0] op_sel_hi:[0,1]
	v_pk_mul_f16 v151, v77, v63 op_sel:[0,0] op_sel_hi:[0,1]
	v_mfma_f32_32x32x16_f16 v[0:15], v[156:159], v[108:111], v[0:15]
	v_pk_fma_f16 v148, v69, v56, v148 op_sel:[0,0,0] op_sel_hi:[0,1,1] neg_lo:[0,0,1] neg_hi:[0,0,1]
	v_pk_fma_f16 v149, v69, v57, v149 op_sel:[0,0,0] op_sel_hi:[0,1,1] neg_lo:[0,0,1] neg_hi:[0,0,1]
	v_pk_fma_f16 v150, v69, v58, v150 op_sel:[0,0,0] op_sel_hi:[0,1,1] neg_lo:[0,0,1] neg_hi:[0,0,1]
	v_pk_fma_f16 v151, v69, v59, v151 op_sel:[0,0,0] op_sel_hi:[0,1,1] neg_lo:[0,0,1] neg_hi:[0,0,1]
	ds_read_b128 v[128:131], v161 offset:12288
	ds_read_b128 v[132:135], v161 offset:13312
	ds_read_b128 v[136:139], v161 offset:14336
	ds_read_b128 v[140:143], v161 offset:15360
	s_waitcnt lgkmcnt(4)
	v_mfma_f32_32x32x16_f16 v[16:31], v[144:147], v[112:115], v[16:31]
	v_pk_mul_f16 v152, v77, v56 op_sel:[1,0] op_sel_hi:[1,1]
	v_pk_mul_f16 v153, v77, v57 op_sel:[1,0] op_sel_hi:[1,1]
	v_pk_mul_f16 v154, v77, v58 op_sel:[1,0] op_sel_hi:[1,1]
	v_pk_mul_f16 v155, v77, v59 op_sel:[1,0] op_sel_hi:[1,1]
	v_mfma_f32_32x32x16_f16 v[0:15], v[144:147], v[116:119], v[0:15]
	v_pk_fma_f16 v152, v69, v60, v152 op_sel:[1,0,0] op_sel_hi:[1,1,1]
	v_pk_fma_f16 v153, v69, v61, v153 op_sel:[1,0,0] op_sel_hi:[1,1,1]
	v_pk_fma_f16 v154, v69, v62, v154 op_sel:[1,0,0] op_sel_hi:[1,1,1]
	v_pk_fma_f16 v155, v69, v63, v155 op_sel:[1,0,0] op_sel_hi:[1,1,1]
	v_mfma_f32_32x32x16_f16 v[16:31], v[148:151], v[120:123], v[16:31]
	v_pk_mul_f16 v156, v77, v60 op_sel:[1,0] op_sel_hi:[1,1]
	v_pk_mul_f16 v157, v77, v61 op_sel:[1,0] op_sel_hi:[1,1]
	v_pk_mul_f16 v158, v77, v62 op_sel:[1,0] op_sel_hi:[1,1]
	v_pk_mul_f16 v159, v77, v63 op_sel:[1,0] op_sel_hi:[1,1]
	v_mfma_f32_32x32x16_f16 v[0:15], v[148:151], v[124:127], v[0:15]
	v_pk_fma_f16 v156, v69, v56, v156 op_sel:[1,0,0] op_sel_hi:[1,1,1] neg_lo:[0,0,1] neg_hi:[0,0,1]
	v_pk_fma_f16 v157, v69, v57, v157 op_sel:[1,0,0] op_sel_hi:[1,1,1] neg_lo:[0,0,1] neg_hi:[0,0,1]
	v_pk_fma_f16 v158, v69, v58, v158 op_sel:[1,0,0] op_sel_hi:[1,1,1] neg_lo:[0,0,1] neg_hi:[0,0,1]
	v_pk_fma_f16 v159, v69, v59, v159 op_sel:[1,0,0] op_sel_hi:[1,1,1] neg_lo:[0,0,1] neg_hi:[0,0,1]
	ds_read_b128 v[80:83], v161 offset:16384
	ds_read_b128 v[84:87], v161 offset:17408
	ds_read_b128 v[88:91], v161 offset:18432
	ds_read_b128 v[92:95], v161 offset:19456
	s_waitcnt lgkmcnt(4)
	v_mfma_f32_32x32x16_f16 v[16:31], v[152:155], v[128:131], v[16:31]
	v_pk_mul_f16 v144, v78, v56 op_sel:[0,0] op_sel_hi:[0,1]
	v_pk_mul_f16 v145, v78, v57 op_sel:[0,0] op_sel_hi:[0,1]
	v_pk_mul_f16 v146, v78, v58 op_sel:[0,0] op_sel_hi:[0,1]
	v_pk_mul_f16 v147, v78, v59 op_sel:[0,0] op_sel_hi:[0,1]
	v_mfma_f32_32x32x16_f16 v[0:15], v[152:155], v[132:135], v[0:15]
	v_pk_fma_f16 v144, v70, v60, v144 op_sel:[0,0,0] op_sel_hi:[0,1,1]
	v_pk_fma_f16 v145, v70, v61, v145 op_sel:[0,0,0] op_sel_hi:[0,1,1]
	v_pk_fma_f16 v146, v70, v62, v146 op_sel:[0,0,0] op_sel_hi:[0,1,1]
	v_pk_fma_f16 v147, v70, v63, v147 op_sel:[0,0,0] op_sel_hi:[0,1,1]
	v_mfma_f32_32x32x16_f16 v[16:31], v[156:159], v[136:139], v[16:31]
	v_pk_mul_f16 v148, v78, v60 op_sel:[0,0] op_sel_hi:[0,1]
	v_pk_mul_f16 v149, v78, v61 op_sel:[0,0] op_sel_hi:[0,1]
	v_pk_mul_f16 v150, v78, v62 op_sel:[0,0] op_sel_hi:[0,1]
	v_pk_mul_f16 v151, v78, v63 op_sel:[0,0] op_sel_hi:[0,1]
	v_mfma_f32_32x32x16_f16 v[0:15], v[156:159], v[140:143], v[0:15]
	v_pk_fma_f16 v148, v70, v56, v148 op_sel:[0,0,0] op_sel_hi:[0,1,1] neg_lo:[0,0,1] neg_hi:[0,0,1]
	v_pk_fma_f16 v149, v70, v57, v149 op_sel:[0,0,0] op_sel_hi:[0,1,1] neg_lo:[0,0,1] neg_hi:[0,0,1]
	v_pk_fma_f16 v150, v70, v58, v150 op_sel:[0,0,0] op_sel_hi:[0,1,1] neg_lo:[0,0,1] neg_hi:[0,0,1]
	v_pk_fma_f16 v151, v70, v59, v151 op_sel:[0,0,0] op_sel_hi:[0,1,1] neg_lo:[0,0,1] neg_hi:[0,0,1]
	ds_read_b128 v[96:99], v161 offset:20480
	ds_read_b128 v[100:103], v161 offset:21504
	ds_read_b128 v[104:107], v161 offset:22528
	ds_read_b128 v[108:111], v161 offset:23552
	s_sub_u32 s17, s17, 1
	s_cmp_eq_u32 s17, 0
	s_cbranch_scc1 .Lk2_epi
.Lk2_h11:
	s_waitcnt lgkmcnt(4)
	v_mfma_f32_32x32x16_f16 v[16:31], v[144:147], v[80:83], v[16:31]
	v_pk_mul_f16 v152, v78, v56 op_sel:[1,0] op_sel_hi:[1,1]
	v_pk_mul_f16 v153, v78, v57 op_sel:[1,0] op_sel_hi:[1,1]
	v_pk_mul_f16 v154, v78, v58 op_sel:[1,0] op_sel_hi:[1,1]
	v_pk_mul_f16 v155, v78, v59 op_sel:[1,0] op_sel_hi:[1,1]
	v_mfma_f32_32x32x16_f16 v[0:15], v[144:147], v[84:87], v[0:15]
	v_pk_fma_f16 v152, v70, v60, v152 op_sel:[1,0,0] op_sel_hi:[1,1,1]
	v_pk_fma_f16 v153, v70, v61, v153 op_sel:[1,0,0] op_sel_hi:[1,1,1]
	v_pk_fma_f16 v154, v70, v62, v154 op_sel:[1,0,0] op_sel_hi:[1,1,1]
	v_pk_fma_f16 v155, v70, v63, v155 op_sel:[1,0,0] op_sel_hi:[1,1,1]
	v_mfma_f32_32x32x16_f16 v[16:31], v[148:151], v[88:91], v[16:31]
	v_pk_mul_f16 v156, v78, v60 op_sel:[1,0] op_sel_hi:[1,1]
	v_pk_mul_f16 v157, v78, v61 op_sel:[1,0] op_sel_hi:[1,1]
	v_pk_mul_f16 v158, v78, v62 op_sel:[1,0] op_sel_hi:[1,1]
	v_pk_mul_f16 v159, v78, v63 op_sel:[1,0] op_sel_hi:[1,1]
	v_mfma_f32_32x32x16_f16 v[0:15], v[148:151], v[92:95], v[0:15]
	v_pk_fma_f16 v156, v70, v56, v156 op_sel:[1,0,0] op_sel_hi:[1,1,1] neg_lo:[0,0,1] neg_hi:[0,0,1]
	v_pk_fma_f16 v157, v70, v57, v157 op_sel:[1,0,0] op_sel_hi:[1,1,1] neg_lo:[0,0,1] neg_hi:[0,0,1]
	v_pk_fma_f16 v158, v70, v58, v158 op_sel:[1,0,0] op_sel_hi:[1,1,1] neg_lo:[0,0,1] neg_hi:[0,0,1]
	v_pk_fma_f16 v159, v70, v59, v159 op_sel:[1,0,0] op_sel_hi:[1,1,1] neg_lo:[0,0,1] neg_hi:[0,0,1]
	ds_read_b128 v[112:115], v161 offset:24576
	ds_read_b128 v[116:119], v161 offset:25600
	ds_read_b128 v[120:123], v161 offset:26624
	ds_read_b128 v[124:127], v161 offset:27648
	s_waitcnt lgkmcnt(4)
	v_mfma_f32_32x32x16_f16 v[16:31], v[152:155], v[96:99], v[16:31]
	v_pk_mul_f16 v144, v79, v56 op_sel:[0,0] op_sel_hi:[0,1]
	v_pk_mul_f16 v145, v79, v57 op_sel:[0,0] op_sel_hi:[0,1]
	v_pk_mul_f16 v146, v79, v58 op_sel:[0,0] op_sel_hi:[0,1]
	v_pk_mul_f16 v147, v79, v59 op_sel:[0,0] op_sel_hi:[0,1]
	v_mfma_f32_32x32x16_f16 v[0:15], v[152:155], v[100:103], v[0:15]
	v_pk_fma_f16 v144, v71, v60, v144 op_sel:[0,0,0] op_sel_hi:[0,1,1]
	v_pk_fma_f16 v145, v71, v61, v145 op_sel:[0,0,0] op_sel_hi:[0,1,1]
	v_pk_fma_f16 v146, v71, v62, v146 op_sel:[0,0,0] op_sel_hi:[0,1,1]
	v_pk_fma_f16 v147, v71, v63, v147 op_sel:[0,0,0] op_sel_hi:[0,1,1]
	v_mfma_f32_32x32x16_f16 v[16:31], v[156:159], v[104:107], v[16:31]
	v_pk_mul_f16 v148, v79, v60 op_sel:[0,0] op_sel_hi:[0,1]
	v_pk_mul_f16 v149, v79, v61 op_sel:[0,0] op_sel_hi:[0,1]
	v_pk_mul_f16 v150, v79, v62 op_sel:[0,0] op_sel_hi:[0,1]
	v_pk_mul_f16 v151, v79, v63 op_sel:[0,0] op_sel_hi:[0,1]
	v_mfma_f32_32x32x16_f16 v[0:15], v[156:159], v[108:111], v[0:15]
	v_pk_fma_f16 v148, v71, v56, v148 op_sel:[0,0,0] op_sel_hi:[0,1,1] neg_lo:[0,0,1] neg_hi:[0,0,1]
	v_pk_fma_f16 v149, v71, v57, v149 op_sel:[0,0,0] op_sel_hi:[0,1,1] neg_lo:[0,0,1] neg_hi:[0,0,1]
	v_pk_fma_f16 v150, v71, v58, v150 op_sel:[0,0,0] op_sel_hi:[0,1,1] neg_lo:[0,0,1] neg_hi:[0,0,1]
	v_pk_fma_f16 v151, v71, v59, v151 op_sel:[0,0,0] op_sel_hi:[0,1,1] neg_lo:[0,0,1] neg_hi:[0,0,1]
	ds_read_b128 v[128:131], v161 offset:28672
	ds_read_b128 v[132:135], v161 offset:29696
	ds_read_b128 v[136:139], v161 offset:30720
	ds_read_b128 v[140:143], v161 offset:31744
	s_add_u32 s19, s19, 0x8000
	s_and_b32 s19, s19, 0x1ffff
	v_add_u32_e32 v161, s19, v160
	s_waitcnt lgkmcnt(4)
	v_mfma_f32_32x32x16_f16 v[16:31], v[144:147], v[112:115], v[16:31]
	v_pk_mul_f16 v152, v79, v56 op_sel:[1,0] op_sel_hi:[1,1]
	v_pk_mul_f16 v153, v79, v57 op_sel:[1,0] op_sel_hi:[1,1]
	v_pk_mul_f16 v154, v79, v58 op_sel:[1,0] op_sel_hi:[1,1]
	v_pk_mul_f16 v155, v79, v59 op_sel:[1,0] op_sel_hi:[1,1]
	v_mfma_f32_32x32x16_f16 v[0:15], v[144:147], v[116:119], v[0:15]
	v_pk_fma_f16 v152, v71, v60, v152 op_sel:[1,0,0] op_sel_hi:[1,1,1]
	v_pk_fma_f16 v153, v71, v61, v153 op_sel:[1,0,0] op_sel_hi:[1,1,1]
	v_pk_fma_f16 v154, v71, v62, v154 op_sel:[1,0,0] op_sel_hi:[1,1,1]
	v_pk_fma_f16 v155, v71, v63, v155 op_sel:[1,0,0] op_sel_hi:[1,1,1]
	v_mfma_f32_32x32x16_f16 v[16:31], v[148:151], v[120:123], v[16:31]
	v_pk_mul_f16 v156, v79, v60 op_sel:[1,0] op_sel_hi:[1,1]
	v_pk_mul_f16 v157, v79, v61 op_sel:[1,0] op_sel_hi:[1,1]
	v_pk_mul_f16 v158, v79, v62 op_sel:[1,0] op_sel_hi:[1,1]
	v_pk_mul_f16 v159, v79, v63 op_sel:[1,0] op_sel_hi:[1,1]
	v_mfma_f32_32x32x16_f16 v[0:15], v[148:151], v[124:127], v[0:15]
	v_pk_fma_f16 v156, v71, v56, v156 op_sel:[1,0,0] op_sel_hi:[1,1,1] neg_lo:[0,0,1] neg_hi:[0,0,1]
	v_pk_fma_f16 v157, v71, v57, v157 op_sel:[1,0,0] op_sel_hi:[1,1,1] neg_lo:[0,0,1] neg_hi:[0,0,1]
	v_pk_fma_f16 v158, v71, v58, v158 op_sel:[1,0,0] op_sel_hi:[1,1,1] neg_lo:[0,0,1] neg_hi:[0,0,1]
	v_pk_fma_f16 v159, v71, v59, v159 op_sel:[1,0,0] op_sel_hi:[1,1,1] neg_lo:[0,0,1] neg_hi:[0,0,1]
	ds_read_b128 v[80:83], v161
	ds_read_b128 v[84:87], v161 offset:1024
	ds_read_b128 v[88:91], v161 offset:2048
	ds_read_b128 v[92:95], v161 offset:3072
	s_waitcnt lgkmcnt(4)
	v_mfma_f32_32x32x16_f16 v[16:31], v[152:155], v[128:131], v[16:31]
	s_waitcnt vmcnt(4)
	v_pk_mul_f16 v144, v48, v32 op_sel:[0,0] op_sel_hi:[0,1]
	v_pk_mul_f16 v145, v48, v33 op_sel:[0,0] op_sel_hi:[0,1]
	v_pk_mul_f16 v146, v48, v34 op_sel:[0,0] op_sel_hi:[0,1]
	v_pk_mul_f16 v147, v48, v35 op_sel:[0,0] op_sel_hi:[0,1]
	v_mfma_f32_32x32x16_f16 v[0:15], v[152:155], v[132:135], v[0:15]
	v_pk_fma_f16 v144, v40, v36, v144 op_sel:[0,0,0] op_sel_hi:[0,1,1]
	v_pk_fma_f16 v145, v40, v37, v145 op_sel:[0,0,0] op_sel_hi:[0,1,1]
	v_pk_fma_f16 v146, v40, v38, v146 op_sel:[0,0,0] op_sel_hi:[0,1,1]
	v_pk_fma_f16 v147, v40, v39, v147 op_sel:[0,0,0] op_sel_hi:[0,1,1]
	v_mfma_f32_32x32x16_f16 v[16:31], v[156:159], v[136:139], v[16:31]
	v_pk_mul_f16 v148, v48, v36 op_sel:[0,0] op_sel_hi:[0,1]
	v_pk_mul_f16 v149, v48, v37 op_sel:[0,0] op_sel_hi:[0,1]
	v_pk_mul_f16 v150, v48, v38 op_sel:[0,0] op_sel_hi:[0,1]
	v_pk_mul_f16 v151, v48, v39 op_sel:[0,0] op_sel_hi:[0,1]
	v_mfma_f32_32x32x16_f16 v[0:15], v[156:159], v[140:143], v[0:15]
	v_pk_fma_f16 v148, v40, v32, v148 op_sel:[0,0,0] op_sel_hi:[0,1,1] neg_lo:[0,0,1] neg_hi:[0,0,1]
	v_pk_fma_f16 v149, v40, v33, v149 op_sel:[0,0,0] op_sel_hi:[0,1,1] neg_lo:[0,0,1] neg_hi:[0,0,1]
	v_pk_fma_f16 v150, v40, v34, v150 op_sel:[0,0,0] op_sel_hi:[0,1,1] neg_lo:[0,0,1] neg_hi:[0,0,1]
	v_pk_fma_f16 v151, v40, v35, v151 op_sel:[0,0,0] op_sel_hi:[0,1,1] neg_lo:[0,0,1] neg_hi:[0,0,1]
	ds_read_b128 v[96:99], v161 offset:4096
	ds_read_b128 v[100:103], v161 offset:5120
	ds_read_b128 v[104:107], v161 offset:6144
	ds_read_b128 v[108:111], v161 offset:7168
	s_sub_u32 s17, s17, 1
	s_cmp_eq_u32 s17, 0
	s_cbranch_scc1 .Lk2_epi
	s_branch .Lk2_s00

	.amdhsa_kernel _Z9feat_gemmPKDF16_S0_PDF16_
		.amdhsa_group_segment_fixed_size 131072
		.amdhsa_private_segment_fixed_size 0
		.amdhsa_kernarg_size 24
		.amdhsa_user_sgpr_count 2
		.amdhsa_user_sgpr_dispatch_ptr 0
		.amdhsa_user_sgpr_queue_ptr 0
		.amdhsa_user_sgpr_kernarg_segment_ptr 1
		.amdhsa_user_sgpr_dispatch_id 0
		.amdhsa_user_sgpr_kernarg_preload_length 0
		.amdhsa_user_sgpr_kernarg_preload_offset 0
		.amdhsa_user_sgpr_private_segment_size 0
		.amdhsa_uses_dynamic_stack 0
		.amdhsa_enable_private_segment 0
		.amdhsa_system_sgpr_workgroup_id_x 1
		.amdhsa_system_sgpr_workgroup_id_y 0
		.amdhsa_system_sgpr_workgroup_id_z 0
		.amdhsa_system_sgpr_workgroup_info 0
		.amdhsa_system_vgpr_workitem_id 0
		.amdhsa_next_free_vgpr 192
		.amdhsa_next_free_sgpr 96
		.amdhsa_accum_offset 192
		.amdhsa_reserve_vcc 1
		.amdhsa_float_round_mode_32 0
		.amdhsa_float_round_mode_16_64 0
		.amdhsa_float_denorm_mode_32 3
		.amdhsa_float_denorm_mode_16_64 3
		.amdhsa_dx10_clamp 1
		.amdhsa_ieee_mode 1
		.amdhsa_fp16_overflow 0
		.amdhsa_tg_split 0
		.amdhsa_exception_fp_ieee_invalid_op 0
		.amdhsa_exception_fp_denorm_src 0
		.amdhsa_exception_fp_ieee_div_zero 0
		.amdhsa_exception_fp_ieee_overflow 0
		.amdhsa_exception_fp_ieee_underflow 0
		.amdhsa_exception_fp_ieee_inexact 0
		.amdhsa_exception_int_div_zero 0
	.end_amdhsa_kernel

amdhsa.kernels:
  - .agpr_count:     0
    .args:
      - .actual_access:  read_only
        .address_space:  global
        .offset:         0
        .size:           8
        .value_kind:     global_buffer
      - .actual_access:  read_only
        .address_space:  global
        .offset:         8
        .size:           8
        .value_kind:     global_buffer
      - .actual_access:  write_only
        .address_space:  global
        .offset:         16
        .size:           8
        .value_kind:     global_buffer
      - .actual_access:  read_only
        .address_space:  global
        .offset:         24
        .size:           8
        .value_kind:     global_buffer
      - .actual_access:  write_only
        .address_space:  global
        .offset:         32
        .size:           8
        .value_kind:     global_buffer
    .group_segment_fixed_size: 43008
    .kernarg_segment_align: 8
    .kernarg_segment_size: 40
    .language:       OpenCL C
    .language_version:
      - 2
      - 0
    .max_flat_workgroup_size: 256
    .name:           _Z15sim_prep_kernelPKfS0_PDF16_S0_S1_
    .private_segment_fixed_size: 0
    .sgpr_count:     43
    .sgpr_spill_count: 0
    .symbol:         _Z15sim_prep_kernelPKfS0_PDF16_S0_S1_.kd
    .uniform_work_group_size: 1
    .uses_dynamic_stack: false
    .vgpr_count:     124
    .vgpr_spill_count: 0
    .wavefront_size: 64
  - .agpr_count:     0
    .args:
      - .address_space:  global
        .offset:         0
        .size:           8
        .value_kind:     global_buffer
      - .address_space:  global
        .offset:         8
        .size:           8
        .value_kind:     global_buffer
      - .actual_access:  write_only
        .address_space:  global
        .offset:         16
        .size:           8
        .value_kind:     global_buffer
    .group_segment_fixed_size: 131072
    .kernarg_segment_align: 8
    .kernarg_segment_size: 24
    .language:       OpenCL C
    .language_version:
      - 2
      - 0
    .max_flat_workgroup_size: 512
    .name:           _Z9feat_gemmPKDF16_S0_PDF16_
    .private_segment_fixed_size: 0
    .sgpr_count:     53
    .sgpr_spill_count: 0
    .symbol:         _Z9feat_gemmPKDF16_S0_PDF16_.kd
    .uniform_work_group_size: 1
    .uses_dynamic_stack: false
    .vgpr_count:     192
    .vgpr_spill_count: 0
    .wavefront_size: 64
  - .agpr_count:     0
    .args:
      - .actual_access:  read_only
        .address_space:  global
        .offset:         0
        .size:           8
        .value_kind:     global_buffer
      - .actual_access:  write_only
        .address_space:  global
        .offset:         8
        .size:           8
        .value_kind:     global_buffer
    .group_segment_fixed_size: 0
    .kernarg_segment_align: 8
    .kernarg_segment_size: 16
    .language:       OpenCL C
    .language_version:
      - 2
      - 0
    .max_flat_workgroup_size: 256
    .name:           _Z13reduce_kernelPKDF16_Pf
    .private_segment_fixed_size: 0
    .sgpr_count:     25
    .sgpr_spill_count: 0
    .symbol:         _Z13reduce_kernelPKDF16_Pf.kd
    .uniform_work_group_size: 1
    .uses_dynamic_stack: false
    .vgpr_count:     78
    .vgpr_spill_count: 0
    .wavefront_size: 64
